# all wq_single weight conversion beyond layer 0 deferred to idle workgroups in the tail rounds of the merge, w_out, FFN1 and FFN2 GEMM phases (2/2/2/3 blocks per idle CU); prologue keeps 432 tasks
# speedup vs baseline: 1.0031x; 1.0031x over previous
.LBB0_109:
	v_readlane_b32 s0, v251, 5
	v_readlane_b32 s6, v251, 11
	v_readlane_b32 s7, v251, 12
	s_add_u32 s0, s6, 0x10f00000
	v_writelane_b32 v252, s0, 12
	s_addc_u32 s0, s7, 0
	v_writelane_b32 v252, s0, 13
	s_add_u32 s0, s6, 0x3c90c0
	v_writelane_b32 v252, s0, 14
	s_addc_u32 s0, s7, 0
	v_writelane_b32 v252, s0, 15
	s_add_u32 s0, s6, 0x3ad0c0
	v_writelane_b32 v252, s0, 16
	s_addc_u32 s0, s7, 0
	v_writelane_b32 v252, s0, 17
	s_add_u32 s0, s6, 0x13800000
	v_writelane_b32 v252, s0, 18
	s_addc_u32 s0, s7, 0
	v_writelane_b32 v252, s0, 19
	s_add_u32 s0, s6, 0x33d0c0
	v_writelane_b32 v252, s0, 20
	s_addc_u32 s0, s7, 0
	v_writelane_b32 v252, s0, 21
	s_add_u32 s0, s6, 0x11700000
	v_writelane_b32 v252, s0, 22
	s_addc_u32 s0, s7, 0
	v_writelane_b32 v252, s0, 23
	s_add_u32 s0, s6, 0x3320c0
	v_mov_b32_e32 v0, 0x135f
	v_readlane_b32 s1, v251, 6
	v_writelane_b32 v252, s0, 24
	s_addc_u32 s0, s7, 0
	v_cmp_gt_i32_e32 vcc, s28, v0
	v_readlane_b32 s2, v251, 7
	v_readlane_b32 s3, v251, 8
	v_readlane_b32 s4, v251, 9
	v_readlane_b32 s5, v251, 10
	v_writelane_b32 v252, s0, 25
	s_and_b64 s[0:1], vcc, exec
	s_mov_b64 s[0:1], s[52:53]
	s_mov_b64 s[2:3], s[54:55]
	s_mov_b64 s[4:5], s[56:57]
	s_mov_b64 s[6:7], s[58:59]
	s_mov_b64 s[8:9], s[60:61]
	s_mov_b64 s[10:11], s[62:63]
	s_mov_b64 s[12:13], s[64:65]
	v_writelane_b32 v252, s0, 26
	s_waitcnt lgkmcnt(0)
	s_barrier
	v_writelane_b32 v252, s1, 27
	v_writelane_b32 v252, s2, 28
	v_writelane_b32 v252, s3, 29
	v_writelane_b32 v252, s4, 30
	v_writelane_b32 v252, s5, 31
	v_writelane_b32 v252, s6, 32
	v_writelane_b32 v252, s7, 33
	v_writelane_b32 v252, s8, 34
	v_writelane_b32 v252, s9, 35
	v_writelane_b32 v252, s10, 36
	v_writelane_b32 v252, s11, 37
	v_writelane_b32 v252, s12, 38
	v_writelane_b32 v252, s13, 39
	v_writelane_b32 v252, s14, 40
	v_writelane_b32 v252, s15, 41
	s_cbranch_scc1 .LBB0_253
	s_mov_b32 s98, s28
	v_readlane_b32 s100, v251, 24
	s_movk_i32 s99, 0x1b0
	s_mov_b32 s101, 0
	s_mov_b32 s0, 0xfffffc00
	s_cmp_lt_u32 s98, 0x11a0
	s_cselect_b32 s0, 0xfffffc00, s0
	s_cmp_lt_u32 s98, 0x1050
	s_cselect_b32 s0, 0xfffffc00, s0
	s_cmp_lt_u32 s98, 0xe70
	s_cselect_b32 s0, 0xfffffc00, s0
	s_cmp_lt_u32 s98, 0xcd0
	s_cselect_b32 s0, 0xfffffc00, s0
	s_cmp_lt_u32 s98, 0xc60
	s_cselect_b32 s0, 0x700, s0
	s_cmp_lt_u32 s98, 0xc40
	s_cselect_b32 s0, 0x6a0, s0
	s_cmp_lt_u32 s98, 0xb60
	s_cselect_b32 s0, 0xfffff600, s0
	s_cmp_lt_u32 s98, 0xaf0
	s_cselect_b32 s0, 0xfffff600, s0
	s_cmp_lt_u32 s98, 0xab0
	s_cselect_b32 s0, 0x890, s0
	s_cmp_lt_u32 s98, 0xa90
	s_cselect_b32 s0, 0x770, s0
	s_cmp_lt_u32 s98, 0x9b0
	s_cselect_b32 s0, 0xfffffeb0, s0
	s_cmp_lt_u32 s98, 0x950
	s_cselect_b32 s0, 0xfffffeb0, s0
	s_cmp_lt_u32 s98, 0x680
	s_cselect_b32 s0, 0xfffffeb0, s0
	s_cmp_lt_u32 s98, 0x530
	s_cselect_b32 s0, 0xfffffeb0, s0
	s_cmp_lt_u32 s98, 0x350
	s_cselect_b32 s0, 0xfffffeb0, s0
	s_cmp_lt_u32 s98, 0x2b0
	s_cselect_b32 s0, 0x1070, s0
	s_cmp_lt_u32 s98, 0x290
	s_cselect_b32 s0, 0xe90, s0
	s_cmp_lt_u32 s98, 0x1b0
	s_cselect_b32 s0, 0x1150, s0
	s_cmp_lt_u32 s98, 0x190
	s_cselect_b32 s0, 0xeb0, s0
	s_cmp_lt_u32 s98, 0xb0
	s_cselect_b32 s0, 0x0, s0
	s_add_i32 s28, s98, s0
	v_lshlrev_b32_e32 v0, 2, v50
	s_add_i32 s0, 0, 0x21000
	v_and_b32_e32 v37, 31, v50
	v_add_u32_e32 v39, s0, v0
	v_cmp_gt_i32_e64 s[0:1], 32, v50
	v_lshlrev_b32_e32 v1, 1, v50
	v_lshlrev_b32_e32 v42, 2, v37
	v_writelane_b32 v252, s0, 42
	v_ashrrev_i32_e32 v40, 3, v50
	v_and_b32_e32 v2, 0xffffffc0, v1
	v_add_u32_e32 v4, 0, v42
	v_writelane_b32 v252, s1, 43
	s_add_i32 s0, 0, 0x21800
	s_movk_i32 s2, 0x84
	v_and_b32_e32 v45, 7, v50
	v_add_u32_e32 v43, s0, v0
	v_add_u32_e32 v82, s0, v42
	v_mad_u64_u32 v[6:7], s[0:1], v2, s2, v[4:5]
	v_mul_lo_u32 v41, v40, s2
	v_lshlrev_b32_e32 v45, 4, v45
	v_add3_u32 v83, v41, v45, 0
	v_lshrrev_b32_e32 v45, 5, v50
	s_movk_i32 s0, 0x2100
	v_and_b32_e32 v35, 28, v0
	v_or_b32_e32 v0, 62, v1
	v_or_b32_e32 v1, 63, v1
	v_mul_lo_u32 v84, v45, s0
	v_mul_lo_u32 v0, v0, s2
	v_mul_lo_u32 v44, v1, s2
	v_or_b32_e32 v10, 2, v2
	v_or_b32_e32 v12, 4, v2
	v_or_b32_e32 v14, 6, v2
	v_or_b32_e32 v16, 8, v2
	v_or_b32_e32 v18, 10, v2
	v_or_b32_e32 v20, 12, v2
	v_or_b32_e32 v22, 14, v2
	v_or_b32_e32 v24, 16, v2
	v_or_b32_e32 v26, 18, v2
	v_or_b32_e32 v28, 20, v2
	v_or_b32_e32 v30, 22, v2
	v_or_b32_e32 v32, 24, v2
	v_or_b32_e32 v34, 26, v2
	v_or_b32_e32 v36, 28, v2
	v_or_b32_e32 v38, 30, v2
	v_ashrrev_i32_e32 v41, 31, v40
	v_or_b32_e32 v42, v84, v42
	v_ashrrev_i32_e32 v3, 31, v2
	v_mov_b32_e32 v8, v2
	v_mov_b32_e32 v1, v2
	v_mov_b32_e32 v5, v10
	v_mov_b32_e32 v7, v12
	v_mov_b32_e32 v9, v14
	v_mov_b32_e32 v11, v16
	v_mov_b32_e32 v13, v18
	v_mov_b32_e32 v15, v20
	v_mov_b32_e32 v17, v22
	v_mov_b32_e32 v19, v24
	v_mov_b32_e32 v21, v26
	v_mov_b32_e32 v23, v28
	v_mov_b32_e32 v25, v30
	v_mov_b32_e32 v27, v32
	v_mov_b32_e32 v29, v34
	v_mov_b32_e32 v31, v36
	v_mov_b32_e32 v33, v38
	v_lshlrev_b64 v[40:41], 2, v[40:41]
	v_add_u32_e32 v42, 0, v42
	v_mov_b32_e32 v45, 0
	v_add_u32_e32 v85, v4, v0
	v_add_u32_e32 v86, v4, v44
	s_branch .LBB0_112
.LBB0_111:
	s_or_b64 exec, exec, s[0:1]
	s_waitcnt lgkmcnt(0)
	s_barrier
	ds_read_b32 v0, v82
	ds_read_b32 v44, v85
	ds_read_b32 v58, v86
	s_mov_b32 s2, 0x42fe0000
	v_add_u32_e32 v57, 0x400, v6
	s_waitcnt lgkmcnt(2)
	v_div_scale_f32 v46, s[0:1], v0, v0, s2
	v_rcp_f32_e32 v47, v46
	v_readlane_b32 s0, v252, 46
	v_readlane_b32 s1, v252, 47
	v_add_u32_e32 v60, 0x800, v6
	v_fma_f32 v48, -v46, v47, 1.0
	v_fmac_f32_e32 v47, v48, v47
	v_div_scale_f32 v48, vcc, s2, v0, s2
	v_mul_f32_e32 v49, v48, v47
	v_fma_f32 v52, -v46, v49, v48
	v_fmac_f32_e32 v49, v52, v47
	v_fma_f32 v46, -v46, v49, v48
	v_div_fmas_f32 v46, v46, v47, v49
	ds_read2_b32 v[48:49], v6 offset1:33
	v_div_fixup_f32 v46, v46, v0, s2
	v_cmp_lt_f32_e32 vcc, 0, v0
	ds_read2_b32 v[52:53], v6 offset0:66 offset1:99
	v_readlane_b32 s28, v252, 44
	v_cndmask_b32_e32 v0, 0, v46, vcc
	s_waitcnt lgkmcnt(1)
	v_mul_f32_e32 v48, v48, v0
	v_rndne_f32_e32 v48, v48
	v_cvt_i32_f32_e32 v54, v48
	v_mul_f32_e32 v48, v0, v49
	v_rndne_f32_e32 v48, v48
	v_cvt_i32_f32_e32 v55, v48
	s_waitcnt lgkmcnt(0)
	v_mul_f32_e32 v48, v0, v52
	v_rndne_f32_e32 v48, v48
	v_cvt_i32_f32_sdwa v52, v48 dst_sel:WORD_1 dst_unused:UNUSED_PAD src0_sel:DWORD
	v_mul_f32_e32 v48, v0, v53
	v_or_b32_e32 v46, s33, v37
	v_rndne_f32_e32 v48, v48
	v_ashrrev_i32_e32 v47, 31, v46
	v_cvt_i32_f32_sdwa v53, v48 dst_sel:BYTE_3 dst_unused:UNUSED_PAD src0_sel:DWORD
	ds_read2_b32 v[48:49], v6 offset0:132 offset1:165
	v_lshlrev_b64 v[46:47], 10, v[46:47]
	v_lshl_add_u64 v[46:47], s[0:1], 0, v[46:47]
	v_lshlrev_b32_e32 v55, 8, v55
	s_mov_b32 s0, 0xc0c0500
	v_perm_b32 v54, v55, v54, s0
	v_and_b32_e32 v52, 0xff0000, v52
	v_or3_b32 v52, v54, v52, v53
	ds_read2_b32 v[54:55], v6 offset0:198 offset1:231
	s_waitcnt lgkmcnt(1)
	v_mul_f32_e32 v48, v0, v48
	v_rndne_f32_e32 v48, v48
	v_cvt_i32_f32_e32 v53, v48
	v_mul_f32_e32 v48, v0, v49
	v_rndne_f32_e32 v48, v48
	v_cvt_i32_f32_e32 v56, v48
	s_waitcnt lgkmcnt(0)
	v_mul_f32_e32 v48, v0, v54
	v_rndne_f32_e32 v48, v48
	v_cvt_i32_f32_sdwa v54, v48 dst_sel:WORD_1 dst_unused:UNUSED_PAD src0_sel:DWORD
	v_mul_f32_e32 v48, v0, v55
	v_rndne_f32_e32 v48, v48
	v_cvt_i32_f32_sdwa v55, v48 dst_sel:BYTE_3 dst_unused:UNUSED_PAD src0_sel:DWORD
	ds_read2_b32 v[48:49], v57 offset0:8 offset1:41
	v_lshlrev_b32_e32 v56, 8, v56
	v_perm_b32 v53, v56, v53, s0
	v_and_b32_e32 v54, 0xff0000, v54
	v_or3_b32 v53, v53, v54, v55
	ds_read2_b32 v[54:55], v57 offset0:74 offset1:107
	s_waitcnt lgkmcnt(1)
	v_mul_f32_e32 v48, v0, v48
	v_rndne_f32_e32 v48, v48
	v_cvt_i32_f32_e32 v56, v48
	v_mul_f32_e32 v48, v0, v49
	v_rndne_f32_e32 v48, v48
	v_cvt_i32_f32_e32 v59, v48
	s_waitcnt lgkmcnt(0)
	v_mul_f32_e32 v48, v0, v54
	v_rndne_f32_e32 v48, v48
	v_cvt_i32_f32_sdwa v54, v48 dst_sel:WORD_1 dst_unused:UNUSED_PAD src0_sel:DWORD
	v_mul_f32_e32 v48, v0, v55
	v_rndne_f32_e32 v48, v48
	v_cvt_i32_f32_sdwa v55, v48 dst_sel:BYTE_3 dst_unused:UNUSED_PAD src0_sel:DWORD
	ds_read2_b32 v[48:49], v57 offset0:140 offset1:173
	v_lshlrev_b32_e32 v59, 8, v59
	v_perm_b32 v56, v59, v56, s0
	v_and_b32_e32 v54, 0xff0000, v54
	v_or3_b32 v54, v56, v54, v55
	ds_read2_b32 v[56:57], v57 offset0:206 offset1:239
	s_waitcnt lgkmcnt(1)
	v_mul_f32_e32 v48, v0, v48
	v_mul_f32_e32 v49, v0, v49
	v_rndne_f32_e32 v48, v48
	v_rndne_f32_e32 v49, v49
	v_cvt_i32_f32_e32 v55, v48
	s_waitcnt lgkmcnt(0)
	v_mul_f32_e32 v48, v0, v56
	v_cvt_i32_f32_e32 v49, v49
	v_rndne_f32_e32 v48, v48
	v_cvt_i32_f32_sdwa v56, v48 dst_sel:WORD_1 dst_unused:UNUSED_PAD src0_sel:DWORD
	v_mul_f32_e32 v48, v0, v57
	v_rndne_f32_e32 v48, v48
	v_cvt_i32_f32_sdwa v57, v48 dst_sel:BYTE_3 dst_unused:UNUSED_PAD src0_sel:DWORD
	v_lshlrev_b32_e32 v59, 8, v49
	ds_read2_b32 v[48:49], v60 offset0:16 offset1:49
	v_perm_b32 v55, v59, v55, s0
	v_and_b32_e32 v56, 0xff0000, v56
	v_lshl_add_u64 v[46:47], v[46:47], 0, v[2:3]
	v_or3_b32 v55, v55, v56, v57
	global_store_dwordx4 v[46:47], v[52:55], off
	ds_read2_b32 v[52:53], v60 offset0:82 offset1:115
	s_waitcnt lgkmcnt(1)
	v_mul_f32_e32 v48, v0, v48
	v_rndne_f32_e32 v48, v48
	v_cvt_i32_f32_e32 v54, v48
	v_mul_f32_e32 v48, v0, v49
	v_rndne_f32_e32 v48, v48
	v_cvt_i32_f32_e32 v55, v48
	s_waitcnt lgkmcnt(0)
	v_mul_f32_e32 v48, v0, v52
	v_rndne_f32_e32 v48, v48
	v_cvt_i32_f32_sdwa v52, v48 dst_sel:WORD_1 dst_unused:UNUSED_PAD src0_sel:DWORD
	v_mul_f32_e32 v48, v0, v53
	v_rndne_f32_e32 v48, v48
	v_cvt_i32_f32_sdwa v53, v48 dst_sel:BYTE_3 dst_unused:UNUSED_PAD src0_sel:DWORD
	ds_read2_b32 v[48:49], v60 offset0:148 offset1:181
	v_lshlrev_b32_e32 v55, 8, v55
	v_perm_b32 v54, v55, v54, s0
	v_and_b32_e32 v52, 0xff0000, v52
	v_or3_b32 v52, v54, v52, v53
	ds_read2_b32 v[54:55], v60 offset0:214 offset1:247
	s_waitcnt lgkmcnt(1)
	v_mul_f32_e32 v48, v0, v48
	v_rndne_f32_e32 v48, v48
	v_cvt_i32_f32_e32 v53, v48
	v_mul_f32_e32 v48, v0, v49
	v_rndne_f32_e32 v48, v48
	v_cvt_i32_f32_e32 v56, v48
	s_waitcnt lgkmcnt(0)
	v_mul_f32_e32 v48, v0, v54
	v_rndne_f32_e32 v48, v48
	v_cvt_i32_f32_sdwa v54, v48 dst_sel:WORD_1 dst_unused:UNUSED_PAD src0_sel:DWORD
	v_mul_f32_e32 v48, v0, v55
	v_rndne_f32_e32 v48, v48
	v_add_u32_e32 v57, 0xc00, v6
	v_cvt_i32_f32_sdwa v55, v48 dst_sel:BYTE_3 dst_unused:UNUSED_PAD src0_sel:DWORD
	ds_read2_b32 v[48:49], v57 offset0:24 offset1:57
	v_lshlrev_b32_e32 v56, 8, v56
	v_perm_b32 v53, v56, v53, s0
	v_and_b32_e32 v54, 0xff0000, v54
	v_or3_b32 v53, v53, v54, v55
	ds_read2_b32 v[54:55], v57 offset0:90 offset1:123
	s_waitcnt lgkmcnt(1)
	v_mul_f32_e32 v48, v0, v48
	v_rndne_f32_e32 v48, v48
	v_cvt_i32_f32_e32 v56, v48
	v_mul_f32_e32 v48, v0, v49
	v_rndne_f32_e32 v48, v48
	v_cvt_i32_f32_e32 v59, v48
	s_waitcnt lgkmcnt(0)
	v_mul_f32_e32 v48, v0, v54
	v_rndne_f32_e32 v48, v48
	v_cvt_i32_f32_sdwa v54, v48 dst_sel:WORD_1 dst_unused:UNUSED_PAD src0_sel:DWORD
	v_mul_f32_e32 v48, v0, v55
	v_rndne_f32_e32 v48, v48
	v_cvt_i32_f32_sdwa v55, v48 dst_sel:BYTE_3 dst_unused:UNUSED_PAD src0_sel:DWORD
	ds_read2_b32 v[48:49], v57 offset0:156 offset1:189
	v_lshlrev_b32_e32 v59, 8, v59
	v_perm_b32 v56, v59, v56, s0
	v_and_b32_e32 v54, 0xff0000, v54
	v_or3_b32 v54, v56, v54, v55
	ds_read2_b32 v[56:57], v57 offset0:222 offset1:255
	s_waitcnt lgkmcnt(1)
	v_mul_f32_e32 v48, v0, v48
	v_mul_f32_e32 v49, v0, v49
	v_rndne_f32_e32 v48, v48
	v_rndne_f32_e32 v49, v49
	v_cvt_i32_f32_e32 v55, v48
	s_waitcnt lgkmcnt(0)
	v_mul_f32_e32 v48, v0, v56
	v_cvt_i32_f32_e32 v49, v49
	v_rndne_f32_e32 v48, v48
	v_cvt_i32_f32_sdwa v56, v48 dst_sel:WORD_1 dst_unused:UNUSED_PAD src0_sel:DWORD
	v_mul_f32_e32 v48, v0, v57
	v_rndne_f32_e32 v48, v48
	v_cvt_i32_f32_sdwa v57, v48 dst_sel:BYTE_3 dst_unused:UNUSED_PAD src0_sel:DWORD
	v_add_u32_e32 v60, 0x1000, v6
	v_lshlrev_b32_e32 v59, 8, v49
	ds_read2_b32 v[48:49], v60 offset0:32 offset1:65
	v_perm_b32 v55, v59, v55, s0
	v_and_b32_e32 v56, 0xff0000, v56
	v_or3_b32 v55, v55, v56, v57
	global_store_dwordx4 v[46:47], v[52:55], off offset:16
	ds_read2_b32 v[52:53], v60 offset0:98 offset1:131
	s_waitcnt lgkmcnt(1)
	v_mul_f32_e32 v48, v0, v48
	v_rndne_f32_e32 v48, v48
	v_cvt_i32_f32_e32 v54, v48
	v_mul_f32_e32 v48, v0, v49
	v_rndne_f32_e32 v48, v48
	v_cvt_i32_f32_e32 v55, v48
	s_waitcnt lgkmcnt(0)
	v_mul_f32_e32 v48, v0, v52
	v_rndne_f32_e32 v48, v48
	v_cvt_i32_f32_sdwa v52, v48 dst_sel:WORD_1 dst_unused:UNUSED_PAD src0_sel:DWORD
	v_mul_f32_e32 v48, v0, v53
	v_rndne_f32_e32 v48, v48
	v_cvt_i32_f32_sdwa v53, v48 dst_sel:BYTE_3 dst_unused:UNUSED_PAD src0_sel:DWORD
	ds_read2_b32 v[48:49], v60 offset0:164 offset1:197
	v_lshlrev_b32_e32 v55, 8, v55
	v_perm_b32 v54, v55, v54, s0
	v_and_b32_e32 v52, 0xff0000, v52
	v_or3_b32 v52, v54, v52, v53
	v_add_u32_e32 v53, 0x1200, v6
	ds_read2_b32 v[54:55], v53 offset0:102 offset1:135
	s_waitcnt lgkmcnt(1)
	v_mul_f32_e32 v48, v0, v48
	v_rndne_f32_e32 v48, v48
	v_cvt_i32_f32_e32 v53, v48
	v_mul_f32_e32 v48, v0, v49
	v_rndne_f32_e32 v48, v48
	v_cvt_i32_f32_e32 v56, v48
	s_waitcnt lgkmcnt(0)
	v_mul_f32_e32 v48, v0, v54
	v_rndne_f32_e32 v48, v48
	v_cvt_i32_f32_sdwa v54, v48 dst_sel:WORD_1 dst_unused:UNUSED_PAD src0_sel:DWORD
	v_mul_f32_e32 v48, v0, v55
	v_rndne_f32_e32 v48, v48
	v_add_u32_e32 v57, 0x1400, v6
	v_cvt_i32_f32_sdwa v55, v48 dst_sel:BYTE_3 dst_unused:UNUSED_PAD src0_sel:DWORD
	ds_read2_b32 v[48:49], v57 offset0:40 offset1:73
	v_lshlrev_b32_e32 v56, 8, v56
	v_perm_b32 v53, v56, v53, s0
	v_and_b32_e32 v54, 0xff0000, v54
	v_or3_b32 v53, v53, v54, v55
	ds_read2_b32 v[54:55], v57 offset0:106 offset1:139
	s_waitcnt lgkmcnt(1)
	v_mul_f32_e32 v48, v0, v48
	v_rndne_f32_e32 v48, v48
	v_cvt_i32_f32_e32 v56, v48
	v_mul_f32_e32 v48, v0, v49
	v_rndne_f32_e32 v48, v48
	v_cvt_i32_f32_e32 v59, v48
	s_waitcnt lgkmcnt(0)
	v_mul_f32_e32 v48, v0, v54
	v_rndne_f32_e32 v48, v48
	v_cvt_i32_f32_sdwa v54, v48 dst_sel:WORD_1 dst_unused:UNUSED_PAD src0_sel:DWORD
	v_mul_f32_e32 v48, v0, v55
	v_rndne_f32_e32 v48, v48
	v_cvt_i32_f32_sdwa v55, v48 dst_sel:BYTE_3 dst_unused:UNUSED_PAD src0_sel:DWORD
	ds_read2_b32 v[48:49], v57 offset0:172 offset1:205
	v_lshlrev_b32_e32 v57, 8, v59
	v_perm_b32 v56, v57, v56, s0
	v_and_b32_e32 v54, 0xff0000, v54
	v_or3_b32 v54, v56, v54, v55
	v_add_u32_e32 v55, 0x1600, v6
	ds_read2_b32 v[56:57], v55 offset0:110 offset1:143
	s_waitcnt lgkmcnt(1)
	v_mul_f32_e32 v48, v0, v48
	v_mul_f32_e32 v49, v0, v49
	v_rndne_f32_e32 v48, v48
	v_rndne_f32_e32 v49, v49
	v_cvt_i32_f32_e32 v55, v48
	s_waitcnt lgkmcnt(0)
	v_mul_f32_e32 v48, v0, v56
	v_cvt_i32_f32_e32 v49, v49
	v_rndne_f32_e32 v48, v48
	v_cvt_i32_f32_sdwa v56, v48 dst_sel:WORD_1 dst_unused:UNUSED_PAD src0_sel:DWORD
	v_mul_f32_e32 v48, v0, v57
	v_rndne_f32_e32 v48, v48
	v_cvt_i32_f32_sdwa v57, v48 dst_sel:BYTE_3 dst_unused:UNUSED_PAD src0_sel:DWORD
	v_add_u32_e32 v60, 0x1800, v6
	v_lshlrev_b32_e32 v59, 8, v49
	ds_read2_b32 v[48:49], v60 offset0:48 offset1:81
	v_perm_b32 v55, v59, v55, s0
	v_and_b32_e32 v56, 0xff0000, v56
	v_or3_b32 v55, v55, v56, v57
	global_store_dwordx4 v[46:47], v[52:55], off offset:32
	ds_read2_b32 v[52:53], v60 offset0:114 offset1:147
	s_waitcnt lgkmcnt(1)
	v_mul_f32_e32 v48, v0, v48
	v_rndne_f32_e32 v48, v48
	v_cvt_i32_f32_e32 v54, v48
	v_mul_f32_e32 v48, v0, v49
	v_rndne_f32_e32 v48, v48
	v_cvt_i32_f32_e32 v55, v48
	s_waitcnt lgkmcnt(0)
	v_mul_f32_e32 v48, v0, v52
	v_rndne_f32_e32 v48, v48
	v_cvt_i32_f32_sdwa v52, v48 dst_sel:WORD_1 dst_unused:UNUSED_PAD src0_sel:DWORD
	v_mul_f32_e32 v48, v0, v53
	v_rndne_f32_e32 v48, v48
	v_cvt_i32_f32_sdwa v53, v48 dst_sel:BYTE_3 dst_unused:UNUSED_PAD src0_sel:DWORD
	ds_read2_b32 v[48:49], v60 offset0:180 offset1:213
	v_lshlrev_b32_e32 v55, 8, v55
	v_perm_b32 v54, v55, v54, s0
	v_and_b32_e32 v52, 0xff0000, v52
	v_or3_b32 v52, v54, v52, v53
	v_add_u32_e32 v53, 0x1a00, v6
	ds_read2_b32 v[54:55], v53 offset0:118 offset1:151
	s_waitcnt lgkmcnt(1)
	v_mul_f32_e32 v48, v0, v48
	v_rndne_f32_e32 v48, v48
	v_cvt_i32_f32_e32 v53, v48
	v_mul_f32_e32 v48, v0, v49
	v_rndne_f32_e32 v48, v48
	v_cvt_i32_f32_e32 v56, v48
	s_waitcnt lgkmcnt(0)
	v_mul_f32_e32 v48, v0, v54
	v_rndne_f32_e32 v48, v48
	v_cvt_i32_f32_sdwa v54, v48 dst_sel:WORD_1 dst_unused:UNUSED_PAD src0_sel:DWORD
	v_mul_f32_e32 v48, v0, v55
	v_rndne_f32_e32 v48, v48
	v_add_u32_e32 v57, 0x1c00, v6
	v_cvt_i32_f32_sdwa v55, v48 dst_sel:BYTE_3 dst_unused:UNUSED_PAD src0_sel:DWORD
	ds_read2_b32 v[48:49], v57 offset0:56 offset1:89
	v_lshlrev_b32_e32 v56, 8, v56
	v_perm_b32 v53, v56, v53, s0
	v_and_b32_e32 v54, 0xff0000, v54
	v_or3_b32 v53, v53, v54, v55
	ds_read2_b32 v[54:55], v57 offset0:122 offset1:155
	s_waitcnt lgkmcnt(1)
	v_mul_f32_e32 v48, v0, v48
	v_rndne_f32_e32 v48, v48
	v_cvt_i32_f32_e32 v56, v48
	v_mul_f32_e32 v48, v0, v49
	v_rndne_f32_e32 v48, v48
	v_cvt_i32_f32_e32 v59, v48
	s_waitcnt lgkmcnt(0)
	v_mul_f32_e32 v48, v0, v54
	v_rndne_f32_e32 v48, v48
	v_cvt_i32_f32_sdwa v54, v48 dst_sel:WORD_1 dst_unused:UNUSED_PAD src0_sel:DWORD
	v_mul_f32_e32 v48, v0, v55
	v_rndne_f32_e32 v48, v48
	v_cvt_i32_f32_sdwa v55, v48 dst_sel:BYTE_3 dst_unused:UNUSED_PAD src0_sel:DWORD
	ds_read2_b32 v[48:49], v57 offset0:188 offset1:221
	v_mul_f32_e32 v44, v0, v44
	v_rndne_f32_e32 v44, v44
	v_cvt_i32_f32_sdwa v44, v44 dst_sel:WORD_1 dst_unused:UNUSED_PAD src0_sel:DWORD
	v_lshlrev_b32_e32 v57, 8, v59
	s_waitcnt lgkmcnt(0)
	v_mul_f32_e32 v49, v0, v49
	v_mul_f32_e32 v48, v0, v48
	v_rndne_f32_e32 v49, v49
	v_rndne_f32_e32 v48, v48
	v_cvt_i32_f32_e32 v49, v49
	v_cvt_i32_f32_e32 v48, v48
	v_mul_f32_e32 v0, v0, v58
	v_rndne_f32_e32 v0, v0
	v_cvt_i32_f32_sdwa v0, v0 dst_sel:BYTE_3 dst_unused:UNUSED_PAD src0_sel:DWORD
	v_lshlrev_b32_e32 v49, 8, v49
	v_perm_b32 v56, v57, v56, s0
	v_perm_b32 v48, v49, v48, s0
	s_add_i32 s98, s98, s100
	v_and_b32_e32 v54, 0xff0000, v54
	v_and_b32_e32 v44, 0xff0000, v44
	s_mov_b32 s0, 0xfffffc00
	s_cmp_lt_u32 s98, 0x11a0
	s_cselect_b32 s0, 0xfffffc00, s0
	s_cmp_lt_u32 s98, 0x1050
	s_cselect_b32 s0, 0xfffffc00, s0
	s_cmp_lt_u32 s98, 0xe70
	s_cselect_b32 s0, 0xfffffc00, s0
	s_cmp_lt_u32 s98, 0xcd0
	s_cselect_b32 s0, 0xfffffc00, s0
	s_cmp_lt_u32 s98, 0xc60
	s_cselect_b32 s0, 0x700, s0
	s_cmp_lt_u32 s98, 0xc40
	s_cselect_b32 s0, 0x6a0, s0
	s_cmp_lt_u32 s98, 0xb60
	s_cselect_b32 s0, 0xfffff600, s0
	s_cmp_lt_u32 s98, 0xaf0
	s_cselect_b32 s0, 0xfffff600, s0
	s_cmp_lt_u32 s98, 0xab0
	s_cselect_b32 s0, 0x890, s0
	s_cmp_lt_u32 s98, 0xa90
	s_cselect_b32 s0, 0x770, s0
	s_cmp_lt_u32 s98, 0x9b0
	s_cselect_b32 s0, 0xfffffeb0, s0
	s_cmp_lt_u32 s98, 0x950
	s_cselect_b32 s0, 0xfffffeb0, s0
	s_cmp_lt_u32 s98, 0x680
	s_cselect_b32 s0, 0xfffffeb0, s0
	s_cmp_lt_u32 s98, 0x530
	s_cselect_b32 s0, 0xfffffeb0, s0
	s_cmp_lt_u32 s98, 0x350
	s_cselect_b32 s0, 0xfffffeb0, s0
	s_cmp_lt_u32 s98, 0x2b0
	s_cselect_b32 s0, 0x1070, s0
	s_cmp_lt_u32 s98, 0x290
	s_cselect_b32 s0, 0xe90, s0
	s_cmp_lt_u32 s98, 0x1b0
	s_cselect_b32 s0, 0x1150, s0
	s_cmp_lt_u32 s98, 0x190
	s_cselect_b32 s0, 0xeb0, s0
	s_cmp_lt_u32 s98, 0xb0
	s_cselect_b32 s0, 0x0, s0
	s_add_i32 s28, s98, s0
	v_or3_b32 v54, v56, v54, v55
	v_or3_b32 v55, v48, v44, v0
	s_cmp_ge_u32 s98, s99
	global_store_dwordx4 v[46:47], v[52:55], off offset:48
	s_barrier
	s_cbranch_scc1 .LBB0_253

.LBB0_1028:
	v_readlane_b32 s98, v251, 3
	v_readlane_b32 s99, v255, 29
	s_cmp_lt_u32 s98, 48
	s_cbranch_scc1 .Lwqd_skip_M
	s_sub_i32 s98, s98, 48
	s_mov_b32 s100, 0
	s_mov_b32 s101, 0
	s_cmp_eq_u32 s99, 0
	s_cselect_b32 s100, 0x1b0, s100
	s_cselect_b32 s101, 0x350, s101
	s_cmp_eq_u32 s99, 1
	s_cselect_b32 s100, 0x950, s100
	s_cselect_b32 s101, 0xaf0, s101
	s_cmp_eq_u32 s99, 2
	s_cselect_b32 s100, 0xcd0, s100
	s_cselect_b32 s101, 0xe70, s101
	s_add_i32 s98, s98, s100
	s_mov_b32 s99, s101
	s_cmp_ge_u32 s98, s99
	s_cbranch_scc1 .Lwqd_skip_M
	s_movk_i32 s100, 208
	s_mov_b32 s101, 3
	v_writelane_b32 v117, s0, 0
	v_writelane_b32 v117, s1, 1
	v_writelane_b32 v117, s2, 2
	v_writelane_b32 v117, s3, 3
	v_writelane_b32 v117, s4, 4
	v_writelane_b32 v117, s5, 5
	v_writelane_b32 v117, s6, 6
	v_writelane_b32 v117, s7, 7
	v_writelane_b32 v117, s8, 8
	v_writelane_b32 v117, s9, 9
	v_writelane_b32 v117, s10, 10
	v_writelane_b32 v117, s11, 11
	v_writelane_b32 v117, s12, 12
	v_writelane_b32 v117, s13, 13
	v_writelane_b32 v117, s14, 14
	v_writelane_b32 v117, s15, 15
	v_writelane_b32 v117, s16, 16
	v_writelane_b32 v117, s17, 17
	v_writelane_b32 v117, s18, 18
	v_writelane_b32 v117, s19, 19
	v_writelane_b32 v117, s20, 20
	v_writelane_b32 v117, s21, 21
	v_writelane_b32 v117, s22, 22
	v_writelane_b32 v117, s23, 23
	v_writelane_b32 v117, s24, 24
	v_writelane_b32 v117, s25, 25
	v_writelane_b32 v117, s26, 26
	v_writelane_b32 v117, s27, 27
	v_writelane_b32 v117, s28, 28
	v_writelane_b32 v117, s29, 29
	v_writelane_b32 v117, s30, 30
	v_writelane_b32 v117, s31, 31
	v_writelane_b32 v117, s32, 32
	v_writelane_b32 v117, s33, 33
	v_writelane_b32 v117, s34, 34
	v_writelane_b32 v117, s35, 35
	v_writelane_b32 v117, s36, 36
	v_writelane_b32 v117, s37, 37
	v_writelane_b32 v117, s38, 38
	v_writelane_b32 v117, s39, 39
	v_writelane_b32 v117, s40, 40
	v_writelane_b32 v117, s41, 41
	v_writelane_b32 v117, s42, 42
	v_writelane_b32 v117, s43, 43
	v_writelane_b32 v117, s44, 44
	v_writelane_b32 v117, s45, 45
	v_writelane_b32 v117, s46, 46
	v_writelane_b32 v117, s47, 47
	v_writelane_b32 v117, s48, 48
	v_writelane_b32 v117, s49, 49
	v_writelane_b32 v117, s50, 50
	v_writelane_b32 v117, s51, 51
	v_writelane_b32 v117, s52, 52
	v_writelane_b32 v117, s53, 53
	v_writelane_b32 v117, s54, 54
	v_writelane_b32 v117, s55, 55
	v_writelane_b32 v117, s56, 56
	v_writelane_b32 v117, s57, 57
	v_writelane_b32 v117, s58, 58
	v_writelane_b32 v117, s59, 59
	v_writelane_b32 v117, s60, 60
	v_writelane_b32 v117, s61, 61
	v_writelane_b32 v117, s62, 62
	v_writelane_b32 v117, s63, 63
	v_writelane_b32 v118, s64, 0
	v_writelane_b32 v118, s65, 1
	v_writelane_b32 v118, s66, 2
	v_writelane_b32 v118, s67, 3
	v_writelane_b32 v118, s68, 4
	v_writelane_b32 v118, s69, 5
	v_writelane_b32 v118, s70, 6
	v_writelane_b32 v118, s71, 7
	v_writelane_b32 v118, s72, 8
	v_writelane_b32 v118, s73, 9
	v_writelane_b32 v118, s74, 10
	v_writelane_b32 v118, s75, 11
	v_writelane_b32 v118, s76, 12
	v_writelane_b32 v118, s77, 13
	v_writelane_b32 v118, s78, 14
	v_writelane_b32 v118, s79, 15
	v_writelane_b32 v118, s80, 16
	v_writelane_b32 v118, s81, 17
	v_writelane_b32 v118, s82, 18
	v_writelane_b32 v118, s83, 19
	v_writelane_b32 v118, s84, 20
	v_writelane_b32 v118, s85, 21
	v_writelane_b32 v118, s86, 22
	v_writelane_b32 v118, s87, 23
	v_writelane_b32 v118, s88, 24
	v_writelane_b32 v118, s89, 25
	v_writelane_b32 v118, s90, 26
	v_writelane_b32 v118, s91, 27
	v_writelane_b32 v118, s92, 28
	v_writelane_b32 v118, s93, 29
	v_writelane_b32 v118, s94, 30
	v_writelane_b32 v118, s95, 31
	v_writelane_b32 v118, s96, 32
	v_writelane_b32 v118, s97, 33
	v_mov_b32_e32 v100, v0
	v_mov_b32_e32 v101, v50
	v_mov_b32_e32 v102, v51
	v_mov_b32_e32 v103, v52
	v_mov_b32_e32 v104, v54
	v_mov_b32_e32 v105, v55
	v_mov_b32_e32 v106, v56
	v_mov_b32_e32 v107, v58
	v_mov_b32_e32 v108, v59
	v_mov_b32_e32 v109, v60
	v_mov_b32_e32 v110, v62
	v_mov_b32_e32 v111, v63
	v_mov_b32_e32 v112, v64
	v_mov_b32_e32 v113, v67
	v_mov_b32_e32 v114, v75
	v_mov_b32_e32 v115, v77
	s_branch .Lwqd_entry

.Lwqd_entry:
	v_mov_b32_e32 v50, v246
	v_mov_b32_e32 v5, 0
	v_readlane_b32 s52, v252, 26
	v_readlane_b32 s53, v252, 27
	s_mov_b32 s0, 0xfffffc00
	s_cmp_lt_u32 s98, 0x11a0
	s_cselect_b32 s0, 0xfffffc00, s0
	s_cmp_lt_u32 s98, 0x1050
	s_cselect_b32 s0, 0xfffffc00, s0
	s_cmp_lt_u32 s98, 0xe70
	s_cselect_b32 s0, 0xfffffc00, s0
	s_cmp_lt_u32 s98, 0xcd0
	s_cselect_b32 s0, 0xfffffc00, s0
	s_cmp_lt_u32 s98, 0xc60
	s_cselect_b32 s0, 0x700, s0
	s_cmp_lt_u32 s98, 0xc40
	s_cselect_b32 s0, 0x6a0, s0
	s_cmp_lt_u32 s98, 0xb60
	s_cselect_b32 s0, 0xfffff600, s0
	s_cmp_lt_u32 s98, 0xaf0
	s_cselect_b32 s0, 0xfffff600, s0
	s_cmp_lt_u32 s98, 0xab0
	s_cselect_b32 s0, 0x890, s0
	s_cmp_lt_u32 s98, 0xa90
	s_cselect_b32 s0, 0x770, s0
	s_cmp_lt_u32 s98, 0x9b0
	s_cselect_b32 s0, 0xfffffeb0, s0
	s_cmp_lt_u32 s98, 0x950
	s_cselect_b32 s0, 0xfffffeb0, s0
	s_cmp_lt_u32 s98, 0x680
	s_cselect_b32 s0, 0xfffffeb0, s0
	s_cmp_lt_u32 s98, 0x530
	s_cselect_b32 s0, 0xfffffeb0, s0
	s_cmp_lt_u32 s98, 0x350
	s_cselect_b32 s0, 0xfffffeb0, s0
	s_cmp_lt_u32 s98, 0x2b0
	s_cselect_b32 s0, 0x1070, s0
	s_cmp_lt_u32 s98, 0x290
	s_cselect_b32 s0, 0xe90, s0
	s_cmp_lt_u32 s98, 0x1b0
	s_cselect_b32 s0, 0x1150, s0
	s_cmp_lt_u32 s98, 0x190
	s_cselect_b32 s0, 0xeb0, s0
	s_cmp_lt_u32 s98, 0xb0
	s_cselect_b32 s0, 0x0, s0
	s_add_i32 s28, s98, s0
	v_lshlrev_b32_e32 v0, 2, v50
	s_add_i32 s0, 0, 0x21000
	v_and_b32_e32 v37, 31, v50
	v_add_u32_e32 v39, s0, v0
	v_cmp_gt_i32_e64 s[0:1], 32, v50
	v_lshlrev_b32_e32 v1, 1, v50
	v_lshlrev_b32_e32 v42, 2, v37
	v_writelane_b32 v116, s0, 0
	v_ashrrev_i32_e32 v40, 3, v50
	v_and_b32_e32 v2, 0xffffffc0, v1
	v_add_u32_e32 v4, 0, v42
	v_writelane_b32 v116, s1, 1
	s_add_i32 s0, 0, 0x21800
	s_movk_i32 s2, 0x84
	v_and_b32_e32 v45, 7, v50
	v_add_u32_e32 v43, s0, v0
	v_add_u32_e32 v82, s0, v42
	v_mad_u64_u32 v[6:7], s[0:1], v2, s2, v[4:5]
	v_mul_lo_u32 v41, v40, s2
	v_lshlrev_b32_e32 v45, 4, v45
	v_add3_u32 v83, v41, v45, 0
	v_lshrrev_b32_e32 v45, 5, v50
	s_movk_i32 s0, 0x2100
	v_and_b32_e32 v35, 28, v0
	v_or_b32_e32 v0, 62, v1
	v_or_b32_e32 v1, 63, v1
	v_mul_lo_u32 v84, v45, s0
	v_mul_lo_u32 v0, v0, s2
	v_mul_lo_u32 v44, v1, s2
	v_or_b32_e32 v10, 2, v2
	v_or_b32_e32 v12, 4, v2
	v_or_b32_e32 v14, 6, v2
	v_or_b32_e32 v16, 8, v2
	v_or_b32_e32 v18, 10, v2
	v_or_b32_e32 v20, 12, v2
	v_or_b32_e32 v22, 14, v2
	v_or_b32_e32 v24, 16, v2
	v_or_b32_e32 v26, 18, v2
	v_or_b32_e32 v28, 20, v2
	v_or_b32_e32 v30, 22, v2
	v_or_b32_e32 v32, 24, v2
	v_or_b32_e32 v34, 26, v2
	v_or_b32_e32 v36, 28, v2
	v_or_b32_e32 v38, 30, v2
	v_ashrrev_i32_e32 v41, 31, v40
	v_or_b32_e32 v42, v84, v42
	v_ashrrev_i32_e32 v3, 31, v2
	v_mov_b32_e32 v8, v2
	v_mov_b32_e32 v1, v2
	v_mov_b32_e32 v5, v10
	v_mov_b32_e32 v7, v12
	v_mov_b32_e32 v9, v14
	v_mov_b32_e32 v11, v16
	v_mov_b32_e32 v13, v18
	v_mov_b32_e32 v15, v20
	v_mov_b32_e32 v17, v22
	v_mov_b32_e32 v19, v24
	v_mov_b32_e32 v21, v26
	v_mov_b32_e32 v23, v28
	v_mov_b32_e32 v25, v30
	v_mov_b32_e32 v27, v32
	v_mov_b32_e32 v29, v34
	v_mov_b32_e32 v31, v36
	v_mov_b32_e32 v33, v38
	v_lshlrev_b64 v[40:41], 2, v[40:41]
	v_add_u32_e32 v42, 0, v42
	v_mov_b32_e32 v45, 0
	v_add_u32_e32 v85, v4, v0
	v_add_u32_e32 v86, v4, v44
	s_branch .Lwqd_112
.Lwqd_111:
	s_or_b64 exec, exec, s[0:1]
	s_waitcnt lgkmcnt(0)
	s_barrier
	ds_read_b32 v0, v82
	ds_read_b32 v44, v85
	ds_read_b32 v58, v86
	s_mov_b32 s2, 0x42fe0000
	v_add_u32_e32 v57, 0x400, v6
	s_waitcnt lgkmcnt(2)
	v_div_scale_f32 v46, s[0:1], v0, v0, s2
	v_rcp_f32_e32 v47, v46
	v_readlane_b32 s0, v116, 4
	v_readlane_b32 s1, v116, 5
	v_add_u32_e32 v60, 0x800, v6
	v_fma_f32 v48, -v46, v47, 1.0
	v_fmac_f32_e32 v47, v48, v47
	v_div_scale_f32 v48, vcc, s2, v0, s2
	v_mul_f32_e32 v49, v48, v47
	v_fma_f32 v52, -v46, v49, v48
	v_fmac_f32_e32 v49, v52, v47
	v_fma_f32 v46, -v46, v49, v48
	v_div_fmas_f32 v46, v46, v47, v49
	ds_read2_b32 v[48:49], v6 offset1:33
	v_div_fixup_f32 v46, v46, v0, s2
	v_cmp_lt_f32_e32 vcc, 0, v0
	ds_read2_b32 v[52:53], v6 offset0:66 offset1:99
	v_readlane_b32 s28, v116, 2
	v_cndmask_b32_e32 v0, 0, v46, vcc
	s_waitcnt lgkmcnt(1)
	v_mul_f32_e32 v48, v48, v0
	v_rndne_f32_e32 v48, v48
	v_cvt_i32_f32_e32 v54, v48
	v_mul_f32_e32 v48, v0, v49
	v_rndne_f32_e32 v48, v48
	v_cvt_i32_f32_e32 v55, v48
	s_waitcnt lgkmcnt(0)
	v_mul_f32_e32 v48, v0, v52
	v_rndne_f32_e32 v48, v48
	v_cvt_i32_f32_sdwa v52, v48 dst_sel:WORD_1 dst_unused:UNUSED_PAD src0_sel:DWORD
	v_mul_f32_e32 v48, v0, v53
	v_or_b32_e32 v46, s33, v37
	v_rndne_f32_e32 v48, v48
	v_ashrrev_i32_e32 v47, 31, v46
	v_cvt_i32_f32_sdwa v53, v48 dst_sel:BYTE_3 dst_unused:UNUSED_PAD src0_sel:DWORD
	ds_read2_b32 v[48:49], v6 offset0:132 offset1:165
	v_lshlrev_b64 v[46:47], 10, v[46:47]
	v_lshl_add_u64 v[46:47], s[0:1], 0, v[46:47]
	v_lshlrev_b32_e32 v55, 8, v55
	s_mov_b32 s0, 0xc0c0500
	v_perm_b32 v54, v55, v54, s0
	v_and_b32_e32 v52, 0xff0000, v52
	v_or3_b32 v52, v54, v52, v53
	ds_read2_b32 v[54:55], v6 offset0:198 offset1:231
	s_waitcnt lgkmcnt(1)
	v_mul_f32_e32 v48, v0, v48
	v_rndne_f32_e32 v48, v48
	v_cvt_i32_f32_e32 v53, v48
	v_mul_f32_e32 v48, v0, v49
	v_rndne_f32_e32 v48, v48
	v_cvt_i32_f32_e32 v56, v48
	s_waitcnt lgkmcnt(0)
	v_mul_f32_e32 v48, v0, v54
	v_rndne_f32_e32 v48, v48
	v_cvt_i32_f32_sdwa v54, v48 dst_sel:WORD_1 dst_unused:UNUSED_PAD src0_sel:DWORD
	v_mul_f32_e32 v48, v0, v55
	v_rndne_f32_e32 v48, v48
	v_cvt_i32_f32_sdwa v55, v48 dst_sel:BYTE_3 dst_unused:UNUSED_PAD src0_sel:DWORD
	ds_read2_b32 v[48:49], v57 offset0:8 offset1:41
	v_lshlrev_b32_e32 v56, 8, v56
	v_perm_b32 v53, v56, v53, s0
	v_and_b32_e32 v54, 0xff0000, v54
	v_or3_b32 v53, v53, v54, v55
	ds_read2_b32 v[54:55], v57 offset0:74 offset1:107
	s_waitcnt lgkmcnt(1)
	v_mul_f32_e32 v48, v0, v48
	v_rndne_f32_e32 v48, v48
	v_cvt_i32_f32_e32 v56, v48
	v_mul_f32_e32 v48, v0, v49
	v_rndne_f32_e32 v48, v48
	v_cvt_i32_f32_e32 v59, v48
	s_waitcnt lgkmcnt(0)
	v_mul_f32_e32 v48, v0, v54
	v_rndne_f32_e32 v48, v48
	v_cvt_i32_f32_sdwa v54, v48 dst_sel:WORD_1 dst_unused:UNUSED_PAD src0_sel:DWORD
	v_mul_f32_e32 v48, v0, v55
	v_rndne_f32_e32 v48, v48
	v_cvt_i32_f32_sdwa v55, v48 dst_sel:BYTE_3 dst_unused:UNUSED_PAD src0_sel:DWORD
	ds_read2_b32 v[48:49], v57 offset0:140 offset1:173
	v_lshlrev_b32_e32 v59, 8, v59
	v_perm_b32 v56, v59, v56, s0
	v_and_b32_e32 v54, 0xff0000, v54
	v_or3_b32 v54, v56, v54, v55
	ds_read2_b32 v[56:57], v57 offset0:206 offset1:239
	s_waitcnt lgkmcnt(1)
	v_mul_f32_e32 v48, v0, v48
	v_mul_f32_e32 v49, v0, v49
	v_rndne_f32_e32 v48, v48
	v_rndne_f32_e32 v49, v49
	v_cvt_i32_f32_e32 v55, v48
	s_waitcnt lgkmcnt(0)
	v_mul_f32_e32 v48, v0, v56
	v_cvt_i32_f32_e32 v49, v49
	v_rndne_f32_e32 v48, v48
	v_cvt_i32_f32_sdwa v56, v48 dst_sel:WORD_1 dst_unused:UNUSED_PAD src0_sel:DWORD
	v_mul_f32_e32 v48, v0, v57
	v_rndne_f32_e32 v48, v48
	v_cvt_i32_f32_sdwa v57, v48 dst_sel:BYTE_3 dst_unused:UNUSED_PAD src0_sel:DWORD
	v_lshlrev_b32_e32 v59, 8, v49
	ds_read2_b32 v[48:49], v60 offset0:16 offset1:49
	v_perm_b32 v55, v59, v55, s0
	v_and_b32_e32 v56, 0xff0000, v56
	v_lshl_add_u64 v[46:47], v[46:47], 0, v[2:3]
	v_or3_b32 v55, v55, v56, v57
	global_store_dwordx4 v[46:47], v[52:55], off
	ds_read2_b32 v[52:53], v60 offset0:82 offset1:115
	s_waitcnt lgkmcnt(1)
	v_mul_f32_e32 v48, v0, v48
	v_rndne_f32_e32 v48, v48
	v_cvt_i32_f32_e32 v54, v48
	v_mul_f32_e32 v48, v0, v49
	v_rndne_f32_e32 v48, v48
	v_cvt_i32_f32_e32 v55, v48
	s_waitcnt lgkmcnt(0)
	v_mul_f32_e32 v48, v0, v52
	v_rndne_f32_e32 v48, v48
	v_cvt_i32_f32_sdwa v52, v48 dst_sel:WORD_1 dst_unused:UNUSED_PAD src0_sel:DWORD
	v_mul_f32_e32 v48, v0, v53
	v_rndne_f32_e32 v48, v48
	v_cvt_i32_f32_sdwa v53, v48 dst_sel:BYTE_3 dst_unused:UNUSED_PAD src0_sel:DWORD
	ds_read2_b32 v[48:49], v60 offset0:148 offset1:181
	v_lshlrev_b32_e32 v55, 8, v55
	v_perm_b32 v54, v55, v54, s0
	v_and_b32_e32 v52, 0xff0000, v52
	v_or3_b32 v52, v54, v52, v53
	ds_read2_b32 v[54:55], v60 offset0:214 offset1:247
	s_waitcnt lgkmcnt(1)
	v_mul_f32_e32 v48, v0, v48
	v_rndne_f32_e32 v48, v48
	v_cvt_i32_f32_e32 v53, v48
	v_mul_f32_e32 v48, v0, v49
	v_rndne_f32_e32 v48, v48
	v_cvt_i32_f32_e32 v56, v48
	s_waitcnt lgkmcnt(0)
	v_mul_f32_e32 v48, v0, v54
	v_rndne_f32_e32 v48, v48
	v_cvt_i32_f32_sdwa v54, v48 dst_sel:WORD_1 dst_unused:UNUSED_PAD src0_sel:DWORD
	v_mul_f32_e32 v48, v0, v55
	v_rndne_f32_e32 v48, v48
	v_add_u32_e32 v57, 0xc00, v6
	v_cvt_i32_f32_sdwa v55, v48 dst_sel:BYTE_3 dst_unused:UNUSED_PAD src0_sel:DWORD
	ds_read2_b32 v[48:49], v57 offset0:24 offset1:57
	v_lshlrev_b32_e32 v56, 8, v56
	v_perm_b32 v53, v56, v53, s0
	v_and_b32_e32 v54, 0xff0000, v54
	v_or3_b32 v53, v53, v54, v55
	ds_read2_b32 v[54:55], v57 offset0:90 offset1:123
	s_waitcnt lgkmcnt(1)
	v_mul_f32_e32 v48, v0, v48
	v_rndne_f32_e32 v48, v48
	v_cvt_i32_f32_e32 v56, v48
	v_mul_f32_e32 v48, v0, v49
	v_rndne_f32_e32 v48, v48
	v_cvt_i32_f32_e32 v59, v48
	s_waitcnt lgkmcnt(0)
	v_mul_f32_e32 v48, v0, v54
	v_rndne_f32_e32 v48, v48
	v_cvt_i32_f32_sdwa v54, v48 dst_sel:WORD_1 dst_unused:UNUSED_PAD src0_sel:DWORD
	v_mul_f32_e32 v48, v0, v55
	v_rndne_f32_e32 v48, v48
	v_cvt_i32_f32_sdwa v55, v48 dst_sel:BYTE_3 dst_unused:UNUSED_PAD src0_sel:DWORD
	ds_read2_b32 v[48:49], v57 offset0:156 offset1:189
	v_lshlrev_b32_e32 v59, 8, v59
	v_perm_b32 v56, v59, v56, s0
	v_and_b32_e32 v54, 0xff0000, v54
	v_or3_b32 v54, v56, v54, v55
	ds_read2_b32 v[56:57], v57 offset0:222 offset1:255
	s_waitcnt lgkmcnt(1)
	v_mul_f32_e32 v48, v0, v48
	v_mul_f32_e32 v49, v0, v49
	v_rndne_f32_e32 v48, v48
	v_rndne_f32_e32 v49, v49
	v_cvt_i32_f32_e32 v55, v48
	s_waitcnt lgkmcnt(0)
	v_mul_f32_e32 v48, v0, v56
	v_cvt_i32_f32_e32 v49, v49
	v_rndne_f32_e32 v48, v48
	v_cvt_i32_f32_sdwa v56, v48 dst_sel:WORD_1 dst_unused:UNUSED_PAD src0_sel:DWORD
	v_mul_f32_e32 v48, v0, v57
	v_rndne_f32_e32 v48, v48
	v_cvt_i32_f32_sdwa v57, v48 dst_sel:BYTE_3 dst_unused:UNUSED_PAD src0_sel:DWORD
	v_add_u32_e32 v60, 0x1000, v6
	v_lshlrev_b32_e32 v59, 8, v49
	ds_read2_b32 v[48:49], v60 offset0:32 offset1:65
	v_perm_b32 v55, v59, v55, s0
	v_and_b32_e32 v56, 0xff0000, v56
	v_or3_b32 v55, v55, v56, v57
	global_store_dwordx4 v[46:47], v[52:55], off offset:16
	ds_read2_b32 v[52:53], v60 offset0:98 offset1:131
	s_waitcnt lgkmcnt(1)
	v_mul_f32_e32 v48, v0, v48
	v_rndne_f32_e32 v48, v48
	v_cvt_i32_f32_e32 v54, v48
	v_mul_f32_e32 v48, v0, v49
	v_rndne_f32_e32 v48, v48
	v_cvt_i32_f32_e32 v55, v48
	s_waitcnt lgkmcnt(0)
	v_mul_f32_e32 v48, v0, v52
	v_rndne_f32_e32 v48, v48
	v_cvt_i32_f32_sdwa v52, v48 dst_sel:WORD_1 dst_unused:UNUSED_PAD src0_sel:DWORD
	v_mul_f32_e32 v48, v0, v53
	v_rndne_f32_e32 v48, v48
	v_cvt_i32_f32_sdwa v53, v48 dst_sel:BYTE_3 dst_unused:UNUSED_PAD src0_sel:DWORD
	ds_read2_b32 v[48:49], v60 offset0:164 offset1:197
	v_lshlrev_b32_e32 v55, 8, v55
	v_perm_b32 v54, v55, v54, s0
	v_and_b32_e32 v52, 0xff0000, v52
	v_or3_b32 v52, v54, v52, v53
	v_add_u32_e32 v53, 0x1200, v6
	ds_read2_b32 v[54:55], v53 offset0:102 offset1:135
	s_waitcnt lgkmcnt(1)
	v_mul_f32_e32 v48, v0, v48
	v_rndne_f32_e32 v48, v48
	v_cvt_i32_f32_e32 v53, v48
	v_mul_f32_e32 v48, v0, v49
	v_rndne_f32_e32 v48, v48
	v_cvt_i32_f32_e32 v56, v48
	s_waitcnt lgkmcnt(0)
	v_mul_f32_e32 v48, v0, v54
	v_rndne_f32_e32 v48, v48
	v_cvt_i32_f32_sdwa v54, v48 dst_sel:WORD_1 dst_unused:UNUSED_PAD src0_sel:DWORD
	v_mul_f32_e32 v48, v0, v55
	v_rndne_f32_e32 v48, v48
	v_add_u32_e32 v57, 0x1400, v6
	v_cvt_i32_f32_sdwa v55, v48 dst_sel:BYTE_3 dst_unused:UNUSED_PAD src0_sel:DWORD
	ds_read2_b32 v[48:49], v57 offset0:40 offset1:73
	v_lshlrev_b32_e32 v56, 8, v56
	v_perm_b32 v53, v56, v53, s0
	v_and_b32_e32 v54, 0xff0000, v54
	v_or3_b32 v53, v53, v54, v55
	ds_read2_b32 v[54:55], v57 offset0:106 offset1:139
	s_waitcnt lgkmcnt(1)
	v_mul_f32_e32 v48, v0, v48
	v_rndne_f32_e32 v48, v48
	v_cvt_i32_f32_e32 v56, v48
	v_mul_f32_e32 v48, v0, v49
	v_rndne_f32_e32 v48, v48
	v_cvt_i32_f32_e32 v59, v48
	s_waitcnt lgkmcnt(0)
	v_mul_f32_e32 v48, v0, v54
	v_rndne_f32_e32 v48, v48
	v_cvt_i32_f32_sdwa v54, v48 dst_sel:WORD_1 dst_unused:UNUSED_PAD src0_sel:DWORD
	v_mul_f32_e32 v48, v0, v55
	v_rndne_f32_e32 v48, v48
	v_cvt_i32_f32_sdwa v55, v48 dst_sel:BYTE_3 dst_unused:UNUSED_PAD src0_sel:DWORD
	ds_read2_b32 v[48:49], v57 offset0:172 offset1:205
	v_lshlrev_b32_e32 v57, 8, v59
	v_perm_b32 v56, v57, v56, s0
	v_and_b32_e32 v54, 0xff0000, v54
	v_or3_b32 v54, v56, v54, v55
	v_add_u32_e32 v55, 0x1600, v6
	ds_read2_b32 v[56:57], v55 offset0:110 offset1:143
	s_waitcnt lgkmcnt(1)
	v_mul_f32_e32 v48, v0, v48
	v_mul_f32_e32 v49, v0, v49
	v_rndne_f32_e32 v48, v48
	v_rndne_f32_e32 v49, v49
	v_cvt_i32_f32_e32 v55, v48
	s_waitcnt lgkmcnt(0)
	v_mul_f32_e32 v48, v0, v56
	v_cvt_i32_f32_e32 v49, v49
	v_rndne_f32_e32 v48, v48
	v_cvt_i32_f32_sdwa v56, v48 dst_sel:WORD_1 dst_unused:UNUSED_PAD src0_sel:DWORD
	v_mul_f32_e32 v48, v0, v57
	v_rndne_f32_e32 v48, v48
	v_cvt_i32_f32_sdwa v57, v48 dst_sel:BYTE_3 dst_unused:UNUSED_PAD src0_sel:DWORD
	v_add_u32_e32 v60, 0x1800, v6
	v_lshlrev_b32_e32 v59, 8, v49
	ds_read2_b32 v[48:49], v60 offset0:48 offset1:81
	v_perm_b32 v55, v59, v55, s0
	v_and_b32_e32 v56, 0xff0000, v56
	v_or3_b32 v55, v55, v56, v57
	global_store_dwordx4 v[46:47], v[52:55], off offset:32
	ds_read2_b32 v[52:53], v60 offset0:114 offset1:147
	s_waitcnt lgkmcnt(1)
	v_mul_f32_e32 v48, v0, v48
	v_rndne_f32_e32 v48, v48
	v_cvt_i32_f32_e32 v54, v48
	v_mul_f32_e32 v48, v0, v49
	v_rndne_f32_e32 v48, v48
	v_cvt_i32_f32_e32 v55, v48
	s_waitcnt lgkmcnt(0)
	v_mul_f32_e32 v48, v0, v52
	v_rndne_f32_e32 v48, v48
	v_cvt_i32_f32_sdwa v52, v48 dst_sel:WORD_1 dst_unused:UNUSED_PAD src0_sel:DWORD
	v_mul_f32_e32 v48, v0, v53
	v_rndne_f32_e32 v48, v48
	v_cvt_i32_f32_sdwa v53, v48 dst_sel:BYTE_3 dst_unused:UNUSED_PAD src0_sel:DWORD
	ds_read2_b32 v[48:49], v60 offset0:180 offset1:213
	v_lshlrev_b32_e32 v55, 8, v55
	v_perm_b32 v54, v55, v54, s0
	v_and_b32_e32 v52, 0xff0000, v52
	v_or3_b32 v52, v54, v52, v53
	v_add_u32_e32 v53, 0x1a00, v6
	ds_read2_b32 v[54:55], v53 offset0:118 offset1:151
	s_waitcnt lgkmcnt(1)
	v_mul_f32_e32 v48, v0, v48
	v_rndne_f32_e32 v48, v48
	v_cvt_i32_f32_e32 v53, v48
	v_mul_f32_e32 v48, v0, v49
	v_rndne_f32_e32 v48, v48
	v_cvt_i32_f32_e32 v56, v48
	s_waitcnt lgkmcnt(0)
	v_mul_f32_e32 v48, v0, v54
	v_rndne_f32_e32 v48, v48
	v_cvt_i32_f32_sdwa v54, v48 dst_sel:WORD_1 dst_unused:UNUSED_PAD src0_sel:DWORD
	v_mul_f32_e32 v48, v0, v55
	v_rndne_f32_e32 v48, v48
	v_add_u32_e32 v57, 0x1c00, v6
	v_cvt_i32_f32_sdwa v55, v48 dst_sel:BYTE_3 dst_unused:UNUSED_PAD src0_sel:DWORD
	ds_read2_b32 v[48:49], v57 offset0:56 offset1:89
	v_lshlrev_b32_e32 v56, 8, v56
	v_perm_b32 v53, v56, v53, s0
	v_and_b32_e32 v54, 0xff0000, v54
	v_or3_b32 v53, v53, v54, v55
	ds_read2_b32 v[54:55], v57 offset0:122 offset1:155
	s_waitcnt lgkmcnt(1)
	v_mul_f32_e32 v48, v0, v48
	v_rndne_f32_e32 v48, v48
	v_cvt_i32_f32_e32 v56, v48
	v_mul_f32_e32 v48, v0, v49
	v_rndne_f32_e32 v48, v48
	v_cvt_i32_f32_e32 v59, v48
	s_waitcnt lgkmcnt(0)
	v_mul_f32_e32 v48, v0, v54
	v_rndne_f32_e32 v48, v48
	v_cvt_i32_f32_sdwa v54, v48 dst_sel:WORD_1 dst_unused:UNUSED_PAD src0_sel:DWORD
	v_mul_f32_e32 v48, v0, v55
	v_rndne_f32_e32 v48, v48
	v_cvt_i32_f32_sdwa v55, v48 dst_sel:BYTE_3 dst_unused:UNUSED_PAD src0_sel:DWORD
	ds_read2_b32 v[48:49], v57 offset0:188 offset1:221
	v_mul_f32_e32 v44, v0, v44
	v_rndne_f32_e32 v44, v44
	v_cvt_i32_f32_sdwa v44, v44 dst_sel:WORD_1 dst_unused:UNUSED_PAD src0_sel:DWORD
	v_lshlrev_b32_e32 v57, 8, v59
	s_waitcnt lgkmcnt(0)
	v_mul_f32_e32 v49, v0, v49
	v_mul_f32_e32 v48, v0, v48
	v_rndne_f32_e32 v49, v49
	v_rndne_f32_e32 v48, v48
	v_cvt_i32_f32_e32 v49, v49
	v_cvt_i32_f32_e32 v48, v48
	v_mul_f32_e32 v0, v0, v58
	v_rndne_f32_e32 v0, v0
	v_cvt_i32_f32_sdwa v0, v0 dst_sel:BYTE_3 dst_unused:UNUSED_PAD src0_sel:DWORD
	v_lshlrev_b32_e32 v49, 8, v49
	v_perm_b32 v56, v57, v56, s0
	v_perm_b32 v48, v49, v48, s0
	s_add_i32 s98, s98, s100
	v_and_b32_e32 v54, 0xff0000, v54
	v_and_b32_e32 v44, 0xff0000, v44
	s_mov_b32 s0, 0xfffffc00
	s_cmp_lt_u32 s98, 0x11a0
	s_cselect_b32 s0, 0xfffffc00, s0
	s_cmp_lt_u32 s98, 0x1050
	s_cselect_b32 s0, 0xfffffc00, s0
	s_cmp_lt_u32 s98, 0xe70
	s_cselect_b32 s0, 0xfffffc00, s0
	s_cmp_lt_u32 s98, 0xcd0
	s_cselect_b32 s0, 0xfffffc00, s0
	s_cmp_lt_u32 s98, 0xc60
	s_cselect_b32 s0, 0x700, s0
	s_cmp_lt_u32 s98, 0xc40
	s_cselect_b32 s0, 0x6a0, s0
	s_cmp_lt_u32 s98, 0xb60
	s_cselect_b32 s0, 0xfffff600, s0
	s_cmp_lt_u32 s98, 0xaf0
	s_cselect_b32 s0, 0xfffff600, s0
	s_cmp_lt_u32 s98, 0xab0
	s_cselect_b32 s0, 0x890, s0
	s_cmp_lt_u32 s98, 0xa90
	s_cselect_b32 s0, 0x770, s0
	s_cmp_lt_u32 s98, 0x9b0
	s_cselect_b32 s0, 0xfffffeb0, s0
	s_cmp_lt_u32 s98, 0x950
	s_cselect_b32 s0, 0xfffffeb0, s0
	s_cmp_lt_u32 s98, 0x680
	s_cselect_b32 s0, 0xfffffeb0, s0
	s_cmp_lt_u32 s98, 0x530
	s_cselect_b32 s0, 0xfffffeb0, s0
	s_cmp_lt_u32 s98, 0x350
	s_cselect_b32 s0, 0xfffffeb0, s0
	s_cmp_lt_u32 s98, 0x2b0
	s_cselect_b32 s0, 0x1070, s0
	s_cmp_lt_u32 s98, 0x290
	s_cselect_b32 s0, 0xe90, s0
	s_cmp_lt_u32 s98, 0x1b0
	s_cselect_b32 s0, 0x1150, s0
	s_cmp_lt_u32 s98, 0x190
	s_cselect_b32 s0, 0xeb0, s0
	s_cmp_lt_u32 s98, 0xb0
	s_cselect_b32 s0, 0x0, s0
	s_add_i32 s28, s98, s0
	v_or3_b32 v54, v56, v54, v55
	v_or3_b32 v55, v48, v44, v0
	s_cmp_ge_u32 s98, s99
	global_store_dwordx4 v[46:47], v[52:55], off offset:48
	s_barrier
	s_cbranch_scc1 .Lwqd_exit

.Lwqd_exit:
	s_mov_b64 exec, -1
	s_cmp_eq_u32 s101, 1
	s_cbranch_scc1 .Lwqd_ret_A
	s_cmp_eq_u32 s101, 2
	s_cbranch_scc1 .Lwqd_ret_F
	s_cmp_eq_u32 s101, 3
	s_cbranch_scc1 .Lwqd_ret_M
	s_cmp_eq_u32 s101, 4
	s_cbranch_scc1 .Lwqd_ret_G
	s_endpgm

.LBB0_1159:
	v_readlane_b32 s98, v251, 3
	v_readlane_b32 s99, v255, 29
	s_cmp_lt_u32 s98, 16
	s_cbranch_scc1 .Lwqd_skip_A
	s_sub_i32 s98, s98, 16
	s_mov_b32 s100, 0
	s_mov_b32 s101, 0
	s_cmp_eq_u32 s99, 0
	s_cselect_b32 s100, 0x350, s100
	s_cselect_b32 s101, 0x530, s101
	s_cmp_eq_u32 s99, 1
	s_cselect_b32 s100, 0xaf0, s100
	s_cselect_b32 s101, 0xcd0, s101
	s_cmp_eq_u32 s99, 2
	s_cselect_b32 s100, 0xe70, s100
	s_cselect_b32 s101, 0x1050, s101
	s_add_i32 s98, s98, s100
	s_mov_b32 s99, s101
	s_cmp_ge_u32 s98, s99
	s_cbranch_scc1 .Lwqd_skip_A
	s_movk_i32 s100, 240
	s_mov_b32 s101, 1
	v_writelane_b32 v117, s0, 0
	v_writelane_b32 v117, s1, 1
	v_writelane_b32 v117, s2, 2
	v_writelane_b32 v117, s3, 3
	v_writelane_b32 v117, s4, 4
	v_writelane_b32 v117, s5, 5
	v_writelane_b32 v117, s6, 6
	v_writelane_b32 v117, s7, 7
	v_writelane_b32 v117, s8, 8
	v_writelane_b32 v117, s9, 9
	v_writelane_b32 v117, s10, 10
	v_writelane_b32 v117, s11, 11
	v_writelane_b32 v117, s12, 12
	v_writelane_b32 v117, s13, 13
	v_writelane_b32 v117, s14, 14
	v_writelane_b32 v117, s15, 15
	v_writelane_b32 v117, s16, 16
	v_writelane_b32 v117, s17, 17
	v_writelane_b32 v117, s18, 18
	v_writelane_b32 v117, s19, 19
	v_writelane_b32 v117, s20, 20
	v_writelane_b32 v117, s21, 21
	v_writelane_b32 v117, s22, 22
	v_writelane_b32 v117, s23, 23
	v_writelane_b32 v117, s24, 24
	v_writelane_b32 v117, s25, 25
	v_writelane_b32 v117, s26, 26
	v_writelane_b32 v117, s27, 27
	v_writelane_b32 v117, s28, 28
	v_writelane_b32 v117, s29, 29
	v_writelane_b32 v117, s30, 30
	v_writelane_b32 v117, s31, 31
	v_writelane_b32 v117, s32, 32
	v_writelane_b32 v117, s33, 33
	v_writelane_b32 v117, s34, 34
	v_writelane_b32 v117, s35, 35
	v_writelane_b32 v117, s36, 36
	v_writelane_b32 v117, s37, 37
	v_writelane_b32 v117, s38, 38
	v_writelane_b32 v117, s39, 39
	v_writelane_b32 v117, s40, 40
	v_writelane_b32 v117, s41, 41
	v_writelane_b32 v117, s42, 42
	v_writelane_b32 v117, s43, 43
	v_writelane_b32 v117, s44, 44
	v_writelane_b32 v117, s45, 45
	v_writelane_b32 v117, s46, 46
	v_writelane_b32 v117, s47, 47
	v_writelane_b32 v117, s48, 48
	v_writelane_b32 v117, s49, 49
	v_writelane_b32 v117, s50, 50
	v_writelane_b32 v117, s51, 51
	v_writelane_b32 v117, s52, 52
	v_writelane_b32 v117, s53, 53
	v_writelane_b32 v117, s54, 54
	v_writelane_b32 v117, s55, 55
	v_writelane_b32 v117, s56, 56
	v_writelane_b32 v117, s57, 57
	v_writelane_b32 v117, s58, 58
	v_writelane_b32 v117, s59, 59
	v_writelane_b32 v117, s60, 60
	v_writelane_b32 v117, s61, 61
	v_writelane_b32 v117, s62, 62
	v_writelane_b32 v117, s63, 63
	v_writelane_b32 v118, s64, 0
	v_writelane_b32 v118, s65, 1
	v_writelane_b32 v118, s66, 2
	v_writelane_b32 v118, s67, 3
	v_writelane_b32 v118, s68, 4
	v_writelane_b32 v118, s69, 5
	v_writelane_b32 v118, s70, 6
	v_writelane_b32 v118, s71, 7
	v_writelane_b32 v118, s72, 8
	v_writelane_b32 v118, s73, 9
	v_writelane_b32 v118, s74, 10
	v_writelane_b32 v118, s75, 11
	v_writelane_b32 v118, s76, 12
	v_writelane_b32 v118, s77, 13
	v_writelane_b32 v118, s78, 14
	v_writelane_b32 v118, s79, 15
	v_writelane_b32 v118, s80, 16
	v_writelane_b32 v118, s81, 17
	v_writelane_b32 v118, s82, 18
	v_writelane_b32 v118, s83, 19
	v_writelane_b32 v118, s84, 20
	v_writelane_b32 v118, s85, 21
	v_writelane_b32 v118, s86, 22
	v_writelane_b32 v118, s87, 23
	v_writelane_b32 v118, s88, 24
	v_writelane_b32 v118, s89, 25
	v_writelane_b32 v118, s90, 26
	v_writelane_b32 v118, s91, 27
	v_writelane_b32 v118, s92, 28
	v_writelane_b32 v118, s93, 29
	v_writelane_b32 v118, s94, 30
	v_writelane_b32 v118, s95, 31
	v_writelane_b32 v118, s96, 32
	v_writelane_b32 v118, s97, 33
	v_mov_b32_e32 v100, v0
	v_mov_b32_e32 v101, v50
	v_mov_b32_e32 v102, v51
	v_mov_b32_e32 v103, v52
	v_mov_b32_e32 v104, v54
	v_mov_b32_e32 v105, v55
	v_mov_b32_e32 v106, v56
	v_mov_b32_e32 v107, v58
	v_mov_b32_e32 v108, v59
	v_mov_b32_e32 v109, v60
	v_mov_b32_e32 v110, v62
	v_mov_b32_e32 v111, v63
	v_mov_b32_e32 v112, v64
	v_mov_b32_e32 v113, v67
	v_mov_b32_e32 v114, v75
	v_mov_b32_e32 v115, v77
	s_branch .Lwqd_entry

.LBB0_1699:
	v_readlane_b32 s98, v251, 3
	v_readlane_b32 s99, v255, 29
	s_cmp_lt_u32 s98, 88
	s_cbranch_scc1 .Lwqd_skip_G
	s_sub_i32 s98, s98, 88
	s_mov_b32 s100, 0
	s_mov_b32 s101, 0
	s_cmp_eq_u32 s99, 0
	s_cselect_b32 s100, 0x530, s100
	s_cselect_b32 s101, 0x680, s101
	s_cmp_eq_u32 s99, 2
	s_cselect_b32 s100, 0x1050, s100
	s_cselect_b32 s101, 0x11a0, s101
	s_add_i32 s98, s98, s100
	s_mov_b32 s99, s101
	s_cmp_ge_u32 s98, s99
	s_cbranch_scc1 .Lwqd_skip_G
	s_movk_i32 s100, 168
	s_mov_b32 s101, 4
	v_writelane_b32 v117, s0, 0
	v_writelane_b32 v117, s1, 1
	v_writelane_b32 v117, s2, 2
	v_writelane_b32 v117, s3, 3
	v_writelane_b32 v117, s4, 4
	v_writelane_b32 v117, s5, 5
	v_writelane_b32 v117, s6, 6
	v_writelane_b32 v117, s7, 7
	v_writelane_b32 v117, s8, 8
	v_writelane_b32 v117, s9, 9
	v_writelane_b32 v117, s10, 10
	v_writelane_b32 v117, s11, 11
	v_writelane_b32 v117, s12, 12
	v_writelane_b32 v117, s13, 13
	v_writelane_b32 v117, s14, 14
	v_writelane_b32 v117, s15, 15
	v_writelane_b32 v117, s16, 16
	v_writelane_b32 v117, s17, 17
	v_writelane_b32 v117, s18, 18
	v_writelane_b32 v117, s19, 19
	v_writelane_b32 v117, s20, 20
	v_writelane_b32 v117, s21, 21
	v_writelane_b32 v117, s22, 22
	v_writelane_b32 v117, s23, 23
	v_writelane_b32 v117, s24, 24
	v_writelane_b32 v117, s25, 25
	v_writelane_b32 v117, s26, 26
	v_writelane_b32 v117, s27, 27
	v_writelane_b32 v117, s28, 28
	v_writelane_b32 v117, s29, 29
	v_writelane_b32 v117, s30, 30
	v_writelane_b32 v117, s31, 31
	v_writelane_b32 v117, s32, 32
	v_writelane_b32 v117, s33, 33
	v_writelane_b32 v117, s34, 34
	v_writelane_b32 v117, s35, 35
	v_writelane_b32 v117, s36, 36
	v_writelane_b32 v117, s37, 37
	v_writelane_b32 v117, s38, 38
	v_writelane_b32 v117, s39, 39
	v_writelane_b32 v117, s40, 40
	v_writelane_b32 v117, s41, 41
	v_writelane_b32 v117, s42, 42
	v_writelane_b32 v117, s43, 43
	v_writelane_b32 v117, s44, 44
	v_writelane_b32 v117, s45, 45
	v_writelane_b32 v117, s46, 46
	v_writelane_b32 v117, s47, 47
	v_writelane_b32 v117, s48, 48
	v_writelane_b32 v117, s49, 49
	v_writelane_b32 v117, s50, 50
	v_writelane_b32 v117, s51, 51
	v_writelane_b32 v117, s52, 52
	v_writelane_b32 v117, s53, 53
	v_writelane_b32 v117, s54, 54
	v_writelane_b32 v117, s55, 55
	v_writelane_b32 v117, s56, 56
	v_writelane_b32 v117, s57, 57
	v_writelane_b32 v117, s58, 58
	v_writelane_b32 v117, s59, 59
	v_writelane_b32 v117, s60, 60
	v_writelane_b32 v117, s61, 61
	v_writelane_b32 v117, s62, 62
	v_writelane_b32 v117, s63, 63
	v_writelane_b32 v118, s64, 0
	v_writelane_b32 v118, s65, 1
	v_writelane_b32 v118, s66, 2
	v_writelane_b32 v118, s67, 3
	v_writelane_b32 v118, s68, 4
	v_writelane_b32 v118, s69, 5
	v_writelane_b32 v118, s70, 6
	v_writelane_b32 v118, s71, 7
	v_writelane_b32 v118, s72, 8
	v_writelane_b32 v118, s73, 9
	v_writelane_b32 v118, s74, 10
	v_writelane_b32 v118, s75, 11
	v_writelane_b32 v118, s76, 12
	v_writelane_b32 v118, s77, 13
	v_writelane_b32 v118, s78, 14
	v_writelane_b32 v118, s79, 15
	v_writelane_b32 v118, s80, 16
	v_writelane_b32 v118, s81, 17
	v_writelane_b32 v118, s82, 18
	v_writelane_b32 v118, s83, 19
	v_writelane_b32 v118, s84, 20
	v_writelane_b32 v118, s85, 21
	v_writelane_b32 v118, s86, 22
	v_writelane_b32 v118, s87, 23
	v_writelane_b32 v118, s88, 24
	v_writelane_b32 v118, s89, 25
	v_writelane_b32 v118, s90, 26
	v_writelane_b32 v118, s91, 27
	v_writelane_b32 v118, s92, 28
	v_writelane_b32 v118, s93, 29
	v_writelane_b32 v118, s94, 30
	v_writelane_b32 v118, s95, 31
	v_writelane_b32 v118, s96, 32
	v_writelane_b32 v118, s97, 33
	v_mov_b32_e32 v100, v0
	v_mov_b32_e32 v101, v50
	v_mov_b32_e32 v102, v51
	v_mov_b32_e32 v103, v52
	v_mov_b32_e32 v104, v54
	v_mov_b32_e32 v105, v55
	v_mov_b32_e32 v106, v56
	v_mov_b32_e32 v107, v58
	v_mov_b32_e32 v108, v59
	v_mov_b32_e32 v109, v60
	v_mov_b32_e32 v110, v62
	v_mov_b32_e32 v111, v63
	v_mov_b32_e32 v112, v64
	v_mov_b32_e32 v113, v67
	v_mov_b32_e32 v114, v75
	v_mov_b32_e32 v115, v77
	s_branch .Lwqd_entry
.Lwqd_ret_G:
	v_mov_b32_e32 v0, v100
	v_mov_b32_e32 v50, v101
	v_mov_b32_e32 v51, v102
	v_mov_b32_e32 v52, v103
	v_mov_b32_e32 v54, v104
	v_mov_b32_e32 v55, v105
	v_mov_b32_e32 v56, v106
	v_mov_b32_e32 v58, v107
	v_mov_b32_e32 v59, v108
	v_mov_b32_e32 v60, v109
	v_mov_b32_e32 v62, v110
	v_mov_b32_e32 v63, v111
	v_mov_b32_e32 v64, v112
	v_mov_b32_e32 v67, v113
	v_mov_b32_e32 v75, v114
	v_mov_b32_e32 v77, v115
	v_readlane_b32 s0, v117, 0
	v_readlane_b32 s1, v117, 1
	v_readlane_b32 s2, v117, 2
	v_readlane_b32 s3, v117, 3
	v_readlane_b32 s4, v117, 4
	v_readlane_b32 s5, v117, 5
	v_readlane_b32 s6, v117, 6
	v_readlane_b32 s7, v117, 7
	v_readlane_b32 s8, v117, 8
	v_readlane_b32 s9, v117, 9
	v_readlane_b32 s10, v117, 10
	v_readlane_b32 s11, v117, 11
	v_readlane_b32 s12, v117, 12
	v_readlane_b32 s13, v117, 13
	v_readlane_b32 s14, v117, 14
	v_readlane_b32 s15, v117, 15
	v_readlane_b32 s16, v117, 16
	v_readlane_b32 s17, v117, 17
	v_readlane_b32 s18, v117, 18
	v_readlane_b32 s19, v117, 19
	v_readlane_b32 s20, v117, 20
	v_readlane_b32 s21, v117, 21
	v_readlane_b32 s22, v117, 22
	v_readlane_b32 s23, v117, 23
	v_readlane_b32 s24, v117, 24
	v_readlane_b32 s25, v117, 25
	v_readlane_b32 s26, v117, 26
	v_readlane_b32 s27, v117, 27
	v_readlane_b32 s28, v117, 28
	v_readlane_b32 s29, v117, 29
	v_readlane_b32 s30, v117, 30
	v_readlane_b32 s31, v117, 31
	v_readlane_b32 s32, v117, 32
	v_readlane_b32 s33, v117, 33
	v_readlane_b32 s34, v117, 34
	v_readlane_b32 s35, v117, 35
	v_readlane_b32 s36, v117, 36
	v_readlane_b32 s37, v117, 37
	v_readlane_b32 s38, v117, 38
	v_readlane_b32 s39, v117, 39
	v_readlane_b32 s40, v117, 40
	v_readlane_b32 s41, v117, 41
	v_readlane_b32 s42, v117, 42
	v_readlane_b32 s43, v117, 43
	v_readlane_b32 s44, v117, 44
	v_readlane_b32 s45, v117, 45
	v_readlane_b32 s46, v117, 46
	v_readlane_b32 s47, v117, 47
	v_readlane_b32 s48, v117, 48
	v_readlane_b32 s49, v117, 49
	v_readlane_b32 s50, v117, 50
	v_readlane_b32 s51, v117, 51
	v_readlane_b32 s52, v117, 52
	v_readlane_b32 s53, v117, 53
	v_readlane_b32 s54, v117, 54
	v_readlane_b32 s55, v117, 55
	v_readlane_b32 s56, v117, 56
	v_readlane_b32 s57, v117, 57
	v_readlane_b32 s58, v117, 58
	v_readlane_b32 s59, v117, 59
	v_readlane_b32 s60, v117, 60
	v_readlane_b32 s61, v117, 61
	v_readlane_b32 s62, v117, 62
	v_readlane_b32 s63, v117, 63
	v_readlane_b32 s64, v118, 0
	v_readlane_b32 s65, v118, 1
	v_readlane_b32 s66, v118, 2
	v_readlane_b32 s67, v118, 3
	v_readlane_b32 s68, v118, 4
	v_readlane_b32 s69, v118, 5
	v_readlane_b32 s70, v118, 6
	v_readlane_b32 s71, v118, 7
	v_readlane_b32 s72, v118, 8
	v_readlane_b32 s73, v118, 9
	v_readlane_b32 s74, v118, 10
	v_readlane_b32 s75, v118, 11
	v_readlane_b32 s76, v118, 12
	v_readlane_b32 s77, v118, 13
	v_readlane_b32 s78, v118, 14
	v_readlane_b32 s79, v118, 15
	v_readlane_b32 s80, v118, 16
	v_readlane_b32 s81, v118, 17
	v_readlane_b32 s82, v118, 18
	v_readlane_b32 s83, v118, 19
	v_readlane_b32 s84, v118, 20
	v_readlane_b32 s85, v118, 21
	v_readlane_b32 s86, v118, 22
	v_readlane_b32 s87, v118, 23
	v_readlane_b32 s88, v118, 24
	v_readlane_b32 s89, v118, 25
	v_readlane_b32 s90, v118, 26
	v_readlane_b32 s91, v118, 27
	v_readlane_b32 s92, v118, 28
	v_readlane_b32 s93, v118, 29
	v_readlane_b32 s94, v118, 30
	v_readlane_b32 s95, v118, 31
	v_readlane_b32 s96, v118, 32
	v_readlane_b32 s97, v118, 33
	s_nop 4
.Lwqd_skip_G:
	s_waitcnt vmcnt(0)
	s_barrier
	s_mov_b64 s[0:1], exec
	v_readlane_b32 s2, v251, 14
	v_readlane_b32 s3, v251, 15
	s_and_b64 s[2:3], s[0:1], s[2:3]
	s_xor_b64 s[0:1], s[2:3], s[0:1]
	s_mov_b64 exec, s[2:3]
	s_cbranch_execz .LBB0_1752
	v_readlane_b32 s2, v255, 9
	s_waitcnt vmcnt(0) expcnt(0) lgkmcnt(0)
	s_nop 0
	v_mov_b32_e32 v1, s2
	ds_read_b32 v3, v1
	v_readlane_b32 s2, v255, 10
	s_waitcnt lgkmcnt(0)
	v_cmp_ne_u32_e32 vcc, 0, v3
	v_mov_b32_e32 v1, s2
	ds_read_b32 v2, v1
	s_cbranch_vccnz .LBB0_1715
	v_readlane_b32 s4, v251, 0
	v_readlane_b32 s5, v251, 1
	s_load_dwordx2 s[2:3], s[4:5], 0x4
	v_readlane_b32 s4, v251, 2
	s_mov_b32 s11, 1
	s_waitcnt lgkmcnt(0)
	s_mul_i32 s10, s2, s4
	s_mul_i32 s10, s10, s3
	s_branch .LBB0_1703

.LBB0_1774:
	v_readlane_b32 s98, v251, 3
	v_readlane_b32 s99, v255, 29
	s_cmp_lt_u32 s98, 16
	s_cbranch_scc1 .Lwqd_skip_F
	s_sub_i32 s98, s98, 16
	s_mov_b32 s100, 0
	s_mov_b32 s101, 0
	s_cmp_eq_u32 s99, 0
	s_cselect_b32 s100, 0x680, s100
	s_cselect_b32 s101, 0x950, s101
	s_cmp_eq_u32 s99, 2
	s_cselect_b32 s100, 0x11a0, s100
	s_cselect_b32 s101, 0x1360, s101
	s_add_i32 s98, s98, s100
	s_mov_b32 s99, s101
	s_cmp_ge_u32 s98, s99
	s_cbranch_scc1 .Lwqd_skip_F
	s_movk_i32 s100, 240
	s_mov_b32 s101, 2
	v_writelane_b32 v117, s0, 0
	v_writelane_b32 v117, s1, 1
	v_writelane_b32 v117, s2, 2
	v_writelane_b32 v117, s3, 3
	v_writelane_b32 v117, s4, 4
	v_writelane_b32 v117, s5, 5
	v_writelane_b32 v117, s6, 6
	v_writelane_b32 v117, s7, 7
	v_writelane_b32 v117, s8, 8
	v_writelane_b32 v117, s9, 9
	v_writelane_b32 v117, s10, 10
	v_writelane_b32 v117, s11, 11
	v_writelane_b32 v117, s12, 12
	v_writelane_b32 v117, s13, 13
	v_writelane_b32 v117, s14, 14
	v_writelane_b32 v117, s15, 15
	v_writelane_b32 v117, s16, 16
	v_writelane_b32 v117, s17, 17
	v_writelane_b32 v117, s18, 18
	v_writelane_b32 v117, s19, 19
	v_writelane_b32 v117, s20, 20
	v_writelane_b32 v117, s21, 21
	v_writelane_b32 v117, s22, 22
	v_writelane_b32 v117, s23, 23
	v_writelane_b32 v117, s24, 24
	v_writelane_b32 v117, s25, 25
	v_writelane_b32 v117, s26, 26
	v_writelane_b32 v117, s27, 27
	v_writelane_b32 v117, s28, 28
	v_writelane_b32 v117, s29, 29
	v_writelane_b32 v117, s30, 30
	v_writelane_b32 v117, s31, 31
	v_writelane_b32 v117, s32, 32
	v_writelane_b32 v117, s33, 33
	v_writelane_b32 v117, s34, 34
	v_writelane_b32 v117, s35, 35
	v_writelane_b32 v117, s36, 36
	v_writelane_b32 v117, s37, 37
	v_writelane_b32 v117, s38, 38
	v_writelane_b32 v117, s39, 39
	v_writelane_b32 v117, s40, 40
	v_writelane_b32 v117, s41, 41
	v_writelane_b32 v117, s42, 42
	v_writelane_b32 v117, s43, 43
	v_writelane_b32 v117, s44, 44
	v_writelane_b32 v117, s45, 45
	v_writelane_b32 v117, s46, 46
	v_writelane_b32 v117, s47, 47
	v_writelane_b32 v117, s48, 48
	v_writelane_b32 v117, s49, 49
	v_writelane_b32 v117, s50, 50
	v_writelane_b32 v117, s51, 51
	v_writelane_b32 v117, s52, 52
	v_writelane_b32 v117, s53, 53
	v_writelane_b32 v117, s54, 54
	v_writelane_b32 v117, s55, 55
	v_writelane_b32 v117, s56, 56
	v_writelane_b32 v117, s57, 57
	v_writelane_b32 v117, s58, 58
	v_writelane_b32 v117, s59, 59
	v_writelane_b32 v117, s60, 60
	v_writelane_b32 v117, s61, 61
	v_writelane_b32 v117, s62, 62
	v_writelane_b32 v117, s63, 63
	v_writelane_b32 v118, s64, 0
	v_writelane_b32 v118, s65, 1
	v_writelane_b32 v118, s66, 2
	v_writelane_b32 v118, s67, 3
	v_writelane_b32 v118, s68, 4
	v_writelane_b32 v118, s69, 5
	v_writelane_b32 v118, s70, 6
	v_writelane_b32 v118, s71, 7
	v_writelane_b32 v118, s72, 8
	v_writelane_b32 v118, s73, 9
	v_writelane_b32 v118, s74, 10
	v_writelane_b32 v118, s75, 11
	v_writelane_b32 v118, s76, 12
	v_writelane_b32 v118, s77, 13
	v_writelane_b32 v118, s78, 14
	v_writelane_b32 v118, s79, 15
	v_writelane_b32 v118, s80, 16
	v_writelane_b32 v118, s81, 17
	v_writelane_b32 v118, s82, 18
	v_writelane_b32 v118, s83, 19
	v_writelane_b32 v118, s84, 20
	v_writelane_b32 v118, s85, 21
	v_writelane_b32 v118, s86, 22
	v_writelane_b32 v118, s87, 23
	v_writelane_b32 v118, s88, 24
	v_writelane_b32 v118, s89, 25
	v_writelane_b32 v118, s90, 26
	v_writelane_b32 v118, s91, 27
	v_writelane_b32 v118, s92, 28
	v_writelane_b32 v118, s93, 29
	v_writelane_b32 v118, s94, 30
	v_writelane_b32 v118, s95, 31
	v_writelane_b32 v118, s96, 32
	v_writelane_b32 v118, s97, 33
	v_mov_b32_e32 v100, v0
	v_mov_b32_e32 v101, v50
	v_mov_b32_e32 v102, v51
	v_mov_b32_e32 v103, v52
	v_mov_b32_e32 v104, v54
	v_mov_b32_e32 v105, v55
	v_mov_b32_e32 v106, v56
	v_mov_b32_e32 v107, v58
	v_mov_b32_e32 v108, v59
	v_mov_b32_e32 v109, v60
	v_mov_b32_e32 v110, v62
	v_mov_b32_e32 v111, v63
	v_mov_b32_e32 v112, v64
	v_mov_b32_e32 v113, v67
	v_mov_b32_e32 v114, v75
	v_mov_b32_e32 v115, v77
	s_branch .Lwqd_entry
.Lwqd_ret_F:
	v_mov_b32_e32 v0, v100
	v_mov_b32_e32 v50, v101
	v_mov_b32_e32 v51, v102
	v_mov_b32_e32 v52, v103
	v_mov_b32_e32 v54, v104
	v_mov_b32_e32 v55, v105
	v_mov_b32_e32 v56, v106
	v_mov_b32_e32 v58, v107
	v_mov_b32_e32 v59, v108
	v_mov_b32_e32 v60, v109
	v_mov_b32_e32 v62, v110
	v_mov_b32_e32 v63, v111
	v_mov_b32_e32 v64, v112
	v_mov_b32_e32 v67, v113
	v_mov_b32_e32 v75, v114
	v_mov_b32_e32 v77, v115
	v_readlane_b32 s0, v117, 0
	v_readlane_b32 s1, v117, 1
	v_readlane_b32 s2, v117, 2
	v_readlane_b32 s3, v117, 3
	v_readlane_b32 s4, v117, 4
	v_readlane_b32 s5, v117, 5
	v_readlane_b32 s6, v117, 6
	v_readlane_b32 s7, v117, 7
	v_readlane_b32 s8, v117, 8
	v_readlane_b32 s9, v117, 9
	v_readlane_b32 s10, v117, 10
	v_readlane_b32 s11, v117, 11
	v_readlane_b32 s12, v117, 12
	v_readlane_b32 s13, v117, 13
	v_readlane_b32 s14, v117, 14
	v_readlane_b32 s15, v117, 15
	v_readlane_b32 s16, v117, 16
	v_readlane_b32 s17, v117, 17
	v_readlane_b32 s18, v117, 18
	v_readlane_b32 s19, v117, 19
	v_readlane_b32 s20, v117, 20
	v_readlane_b32 s21, v117, 21
	v_readlane_b32 s22, v117, 22
	v_readlane_b32 s23, v117, 23
	v_readlane_b32 s24, v117, 24
	v_readlane_b32 s25, v117, 25
	v_readlane_b32 s26, v117, 26
	v_readlane_b32 s27, v117, 27
	v_readlane_b32 s28, v117, 28
	v_readlane_b32 s29, v117, 29
	v_readlane_b32 s30, v117, 30
	v_readlane_b32 s31, v117, 31
	v_readlane_b32 s32, v117, 32
	v_readlane_b32 s33, v117, 33
	v_readlane_b32 s34, v117, 34
	v_readlane_b32 s35, v117, 35
	v_readlane_b32 s36, v117, 36
	v_readlane_b32 s37, v117, 37
	v_readlane_b32 s38, v117, 38
	v_readlane_b32 s39, v117, 39
	v_readlane_b32 s40, v117, 40
	v_readlane_b32 s41, v117, 41
	v_readlane_b32 s42, v117, 42
	v_readlane_b32 s43, v117, 43
	v_readlane_b32 s44, v117, 44
	v_readlane_b32 s45, v117, 45
	v_readlane_b32 s46, v117, 46
	v_readlane_b32 s47, v117, 47
	v_readlane_b32 s48, v117, 48
	v_readlane_b32 s49, v117, 49
	v_readlane_b32 s50, v117, 50
	v_readlane_b32 s51, v117, 51
	v_readlane_b32 s52, v117, 52
	v_readlane_b32 s53, v117, 53
	v_readlane_b32 s54, v117, 54
	v_readlane_b32 s55, v117, 55
	v_readlane_b32 s56, v117, 56
	v_readlane_b32 s57, v117, 57
	v_readlane_b32 s58, v117, 58
	v_readlane_b32 s59, v117, 59
	v_readlane_b32 s60, v117, 60
	v_readlane_b32 s61, v117, 61
	v_readlane_b32 s62, v117, 62
	v_readlane_b32 s63, v117, 63
	v_readlane_b32 s64, v118, 0
	v_readlane_b32 s65, v118, 1
	v_readlane_b32 s66, v118, 2
	v_readlane_b32 s67, v118, 3
	v_readlane_b32 s68, v118, 4
	v_readlane_b32 s69, v118, 5
	v_readlane_b32 s70, v118, 6
	v_readlane_b32 s71, v118, 7
	v_readlane_b32 s72, v118, 8
	v_readlane_b32 s73, v118, 9
	v_readlane_b32 s74, v118, 10
	v_readlane_b32 s75, v118, 11
	v_readlane_b32 s76, v118, 12
	v_readlane_b32 s77, v118, 13
	v_readlane_b32 s78, v118, 14
	v_readlane_b32 s79, v118, 15
	v_readlane_b32 s80, v118, 16
	v_readlane_b32 s81, v118, 17
	v_readlane_b32 s82, v118, 18
	v_readlane_b32 s83, v118, 19
	v_readlane_b32 s84, v118, 20
	v_readlane_b32 s85, v118, 21
	v_readlane_b32 s86, v118, 22
	v_readlane_b32 s87, v118, 23
	v_readlane_b32 s88, v118, 24
	v_readlane_b32 s89, v118, 25
	v_readlane_b32 s90, v118, 26
	v_readlane_b32 s91, v118, 27
	v_readlane_b32 s92, v118, 28
	v_readlane_b32 s93, v118, 29
	v_readlane_b32 s94, v118, 30
	v_readlane_b32 s95, v118, 31
	v_readlane_b32 s96, v118, 32
	v_readlane_b32 s97, v118, 33
	s_nop 4
.Lwqd_skip_F:
	s_waitcnt vmcnt(0)
	s_barrier
	s_mov_b64 s[0:1], exec
	v_readlane_b32 s2, v251, 14
	v_readlane_b32 s3, v251, 15
	s_and_b64 s[2:3], s[0:1], s[2:3]
	s_mov_b64 exec, s[2:3]
	s_cbranch_execnz .LBB0_1775
	s_getpc_b64 s[98:99]
